# baseline (speedup 1.0000x reference)
.LBB1_33:
	s_mov_b32 s5, 0
	v_lshl_add_u64 v[168:169], v[154:155], 0, s[4:5]
	global_load_dwordx4 v[154:157], v[168:169], off
	ds_read_b128 v[50:53], v179 offset:33792
	ds_read_b128 v[54:57], v179 offset:33824
	ds_read_b128 v[58:61], v179 offset:33856
	ds_read_b128 v[62:65], v179 offset:33888
	ds_read_b128 v[180:183], v179 offset:33920
	ds_read_b128 v[184:187], v179 offset:33952
	s_waitcnt lgkmcnt(5)
	v_mfma_f32_32x32x16_f16 v[34:49], v[122:125], v[50:53], v[2:17]
	ds_read_b128 v[190:193], v179 offset:33984
	v_cvt_pk_f16_f32 v174, v18, v19
	v_cvt_pk_f16_f32 v175, v20, v21
	s_waitcnt lgkmcnt(5)
	v_mfma_f32_32x32x16_f16 v[34:49], v[98:101], v[54:57], v[34:49]
	ds_read_b128 v[18:21], v179 offset:34016
	v_exp_f16_e64 v50, v174 clamp
	v_exp_f16_e64 v51, v175 clamp
	v_exp_f16_sdwa v50, v174 clamp dst_sel:WORD_1 dst_unused:UNUSED_PRESERVE src0_sel:WORD_1
	v_exp_f16_sdwa v51, v175 clamp dst_sel:WORD_1 dst_unused:UNUSED_PRESERVE src0_sel:WORD_1
	s_nop 0
	s_waitcnt lgkmcnt(5)
	v_mfma_f32_32x32x16_f16 v[34:49], v[114:117], v[58:61], v[34:49]
	ds_read_b128 v[194:197], v179 offset:34048
	s_movk_i32 s5, 0x3dc5
	v_mov_b32_e32 v188, 0xbdc5
	v_pk_fma_f16 v51, v51, s5, v188 op_sel_hi:[1,0,0]
	v_pk_fma_f16 v50, v50, s5, v188 op_sel_hi:[1,0,0]
	v_pk_max_f16 v51, v175, v51
	v_pk_max_f16 v50, v174, v50
	s_waitcnt lgkmcnt(5)
	v_mfma_f32_32x32x16_f16 v[34:49], v[86:89], v[62:65], v[34:49]
	ds_read_b128 v[200:203], v179 offset:34080
	v_cvt_pk_f16_f32 v52, v22, v23
	v_cvt_pk_f16_f32 v53, v24, v25
	s_waitcnt lgkmcnt(5)
	v_mfma_f32_32x32x16_f16 v[34:49], v[126:129], v[180:183], v[34:49]
	ds_read_b128 v[22:25], v179 offset:34112
	v_exp_f16_e64 v54, v52 clamp
	v_exp_f16_e64 v55, v53 clamp
	v_exp_f16_sdwa v54, v52 clamp dst_sel:WORD_1 dst_unused:UNUSED_PRESERVE src0_sel:WORD_1
	v_exp_f16_sdwa v55, v53 clamp dst_sel:WORD_1 dst_unused:UNUSED_PRESERVE src0_sel:WORD_1
	s_nop 0
	s_waitcnt lgkmcnt(5)
	v_mfma_f32_32x32x16_f16 v[34:49], v[90:93], v[184:187], v[34:49]
	ds_read_b128 v[180:183], v179 offset:34144
	v_pk_fma_f16 v55, v55, s5, v188 op_sel_hi:[1,0,0]
	v_pk_fma_f16 v54, v54, s5, v188 op_sel_hi:[1,0,0]
	v_pk_max_f16 v53, v53, v55
	v_pk_max_f16 v52, v52, v54
	s_waitcnt lgkmcnt(5)
	v_mfma_f32_32x32x16_f16 v[34:49], v[118:121], v[190:193], v[34:49]
	ds_read_b128 v[184:187], v179 offset:34176
	v_cvt_pk_f16_f32 v174, v26, v27
	v_cvt_pk_f16_f32 v175, v28, v29
	v_mfma_f32_16x16x32_f16 v[62:65], v[70:73], v[50:53], 0
	s_waitcnt lgkmcnt(5)
	v_mfma_f32_32x32x16_f16 v[34:49], v[78:81], v[18:21], v[34:49]
	ds_read_b128 v[26:29], v179 offset:34208
	v_exp_f16_e64 v190, v174 clamp
	v_exp_f16_e64 v191, v175 clamp
	v_exp_f16_sdwa v190, v174 clamp dst_sel:WORD_1 dst_unused:UNUSED_PRESERVE src0_sel:WORD_1
	v_exp_f16_sdwa v191, v175 clamp dst_sel:WORD_1 dst_unused:UNUSED_PRESERVE src0_sel:WORD_1
	s_nop 0
	s_waitcnt lgkmcnt(5)
	v_mfma_f32_32x32x16_f16 v[34:49], v[102:105], v[194:197], v[34:49]
	ds_read_b128 v[18:21], v179 offset:34240
	v_pk_fma_f16 v191, v191, s5, v188 op_sel_hi:[1,0,0]
	s_nop 0
	v_pk_max_f16 v191, v175, v191
	v_pk_fma_f16 v175, v190, s5, v188 op_sel_hi:[1,0,0]
	s_nop 0
	v_pk_max_f16 v190, v174, v175
	s_waitcnt lgkmcnt(5)
	v_mfma_f32_32x32x16_f16 v[34:49], v[74:77], v[200:203], v[34:49]
	ds_read_b128 v[194:197], v179 offset:34272
	v_cvt_pk_f16_f32 v30, v30, v31
	v_cvt_pk_f16_f32 v31, v32, v33
	s_waitcnt lgkmcnt(5)
	v_mfma_f32_32x32x16_f16 v[34:49], v[106:109], v[22:25], v[34:49]
	v_exp_f16_e64 v32, v30 clamp
	v_exp_f16_e64 v33, v31 clamp
	v_exp_f16_sdwa v32, v30 clamp dst_sel:WORD_1 dst_unused:UNUSED_PRESERVE src0_sel:WORD_1
	v_exp_f16_sdwa v33, v31 clamp dst_sel:WORD_1 dst_unused:UNUSED_PRESERVE src0_sel:WORD_1
	s_nop 0
	s_waitcnt lgkmcnt(4)
	v_mfma_f32_32x32x16_f16 v[34:49], v[82:85], v[180:183], v[34:49]
	v_pk_fma_f16 v22, v33, s5, v188 op_sel_hi:[1,0,0]
	s_nop 0
	v_pk_max_f16 v193, v31, v22
	v_pk_fma_f16 v22, v32, s5, v188 op_sel_hi:[1,0,0]
	s_nop 0
	v_pk_max_f16 v192, v30, v22
	s_waitcnt lgkmcnt(3)
	v_mfma_f32_32x32x16_f16 v[34:49], v[110:113], v[184:187], v[34:49]
	s_waitcnt vmcnt(2)
	v_pk_add_f16 v24, v158, v146
	v_pk_add_f16 v25, v159, v147
	s_nop 0
	v_pk_mul_f16 v22, v160, v148 clamp
	v_pk_mul_f16 v23, v161, v149 clamp
	v_pk_max_f16 v22, v24, v22
	v_pk_max_f16 v23, v25, v23
	ds_write_b64 v189, v[22:23]
	v_mfma_f32_16x16x32_f16 v[62:65], v[66:69], v[190:193], v[62:65]
	s_waitcnt lgkmcnt(3)
	v_mfma_f32_32x32x16_f16 v[34:49], v[94:97], v[26:29], v[34:49]
	v_pk_add_f16 v24, v158, v138
	v_pk_add_f16 v25, v159, v139
	s_nop 0
	v_pk_mul_f16 v22, v160, v140 clamp
	v_pk_mul_f16 v23, v161, v141 clamp
	v_pk_max_f16 v22, v24, v22
	v_pk_max_f16 v23, v25, v23
	ds_write_b64 v189, v[22:23] offset:528
	s_waitcnt lgkmcnt(3)
	v_mfma_f32_32x32x16_f16 v[34:49], v[134:137], v[18:21], v[34:49]
	v_pk_add_f16 v24, v158, v150
	v_pk_add_f16 v25, v159, v151
	s_nop 0
	v_pk_mul_f16 v22, v160, v152 clamp
	v_pk_mul_f16 v23, v161, v153 clamp
	v_pk_max_f16 v22, v24, v22
	v_pk_max_f16 v23, v25, v23
	ds_write_b64 v189, v[22:23] offset:1056
	s_waitcnt lgkmcnt(3)
	v_mfma_f32_32x32x16_f16 v[34:49], v[130:133], v[194:197], v[34:49]
	v_pk_add_f16 v20, v158, v142
	v_pk_add_f16 v21, v159, v143
	s_nop 0
	v_pk_mul_f16 v18, v160, v144 clamp
	v_pk_mul_f16 v19, v161, v145 clamp
	v_pk_max_f16 v18, v20, v18
	v_pk_max_f16 v19, v21, v19
	ds_write_b64 v189, v[18:19] offset:1584
	v_mov_b32_e32 v18, 0x12400
	v_lshl_add_u32 v201, v170, 2, v18
	v_mov_b32_e32 v18, 0x12408
	v_lshl_add_u32 v18, v167, 2, v18
	s_mov_b32 s5, 0x12400
	v_add3_u32 v18, v171, v172, s5
	ds_write2_b32 v201, v62, v63 offset1:1
	s_and_saveexec_b64 s[6:7], s[0:1]
	ds_write2_b32 v201, v64, v65 offset0:2 offset1:3
	s_or_b64 exec, exec, s[6:7]
	s_mov_b32 s5, 0
	v_lshl_add_u64 v[168:169], v[168:169], 0, s[4:5]
	global_load_dwordx4 v[158:161], v[168:169], off
	ds_read_b128 v[50:53], v179 offset:50688
	ds_read_b128 v[54:57], v179 offset:50720
	ds_read_b128 v[58:61], v179 offset:50752
	ds_read_b128 v[62:65], v179 offset:50784
	ds_read_b128 v[180:183], v179 offset:50816
	ds_read_b128 v[184:187], v179 offset:50848
	s_waitcnt lgkmcnt(5)
	v_mfma_f32_32x32x16_f16 v[18:33], v[122:125], v[50:53], v[2:17]
	ds_read_b128 v[190:193], v179 offset:50880
	v_cvt_pk_f16_f32 v174, v34, v35
	v_cvt_pk_f16_f32 v175, v36, v37
	s_waitcnt lgkmcnt(5)
	v_mfma_f32_32x32x16_f16 v[18:33], v[98:101], v[54:57], v[18:33]
	ds_read_b128 v[34:37], v179 offset:50912
	v_exp_f16_e64 v50, v174 clamp
	v_exp_f16_e64 v51, v175 clamp
	v_exp_f16_sdwa v50, v174 clamp dst_sel:WORD_1 dst_unused:UNUSED_PRESERVE src0_sel:WORD_1
	v_exp_f16_sdwa v51, v175 clamp dst_sel:WORD_1 dst_unused:UNUSED_PRESERVE src0_sel:WORD_1
	s_nop 0
	s_waitcnt lgkmcnt(5)
	v_mfma_f32_32x32x16_f16 v[18:33], v[114:117], v[58:61], v[18:33]
	ds_read_b128 v[194:197], v179 offset:50944
	s_movk_i32 s5, 0x3dc5
	v_mov_b32_e32 v188, 0xbdc5
	v_pk_fma_f16 v51, v51, s5, v188 op_sel_hi:[1,0,0]
	v_pk_fma_f16 v50, v50, s5, v188 op_sel_hi:[1,0,0]
	v_pk_max_f16 v51, v175, v51
	v_pk_max_f16 v50, v174, v50
	s_waitcnt lgkmcnt(5)
	v_mfma_f32_32x32x16_f16 v[18:33], v[86:89], v[62:65], v[18:33]
	ds_read_b128 v[202:205], v179 offset:50976
	v_cvt_pk_f16_f32 v52, v38, v39
	v_cvt_pk_f16_f32 v53, v40, v41
	s_waitcnt lgkmcnt(5)
	v_mfma_f32_32x32x16_f16 v[18:33], v[126:129], v[180:183], v[18:33]
	ds_read_b128 v[38:41], v179 offset:51008
	v_exp_f16_e64 v54, v52 clamp
	v_exp_f16_e64 v55, v53 clamp
	v_exp_f16_sdwa v54, v52 clamp dst_sel:WORD_1 dst_unused:UNUSED_PRESERVE src0_sel:WORD_1
	v_exp_f16_sdwa v55, v53 clamp dst_sel:WORD_1 dst_unused:UNUSED_PRESERVE src0_sel:WORD_1
	s_nop 0
	s_waitcnt lgkmcnt(5)
	v_mfma_f32_32x32x16_f16 v[18:33], v[90:93], v[184:187], v[18:33]
	ds_read_b128 v[180:183], v179 offset:51040
	v_pk_fma_f16 v55, v55, s5, v188 op_sel_hi:[1,0,0]
	v_pk_fma_f16 v54, v54, s5, v188 op_sel_hi:[1,0,0]
	v_pk_max_f16 v53, v53, v55
	v_pk_max_f16 v52, v52, v54
	s_waitcnt lgkmcnt(5)
	v_mfma_f32_32x32x16_f16 v[18:33], v[118:121], v[190:193], v[18:33]
	ds_read_b128 v[184:187], v179 offset:51072
	v_cvt_pk_f16_f32 v174, v42, v43
	v_cvt_pk_f16_f32 v175, v44, v45
	v_mfma_f32_16x16x32_f16 v[62:65], v[70:73], v[50:53], 0
	s_waitcnt lgkmcnt(5)
	v_mfma_f32_32x32x16_f16 v[18:33], v[78:81], v[34:37], v[18:33]
	ds_read_b128 v[42:45], v179 offset:51104
	v_exp_f16_e64 v190, v174 clamp
	v_exp_f16_e64 v191, v175 clamp
	v_exp_f16_sdwa v190, v174 clamp dst_sel:WORD_1 dst_unused:UNUSED_PRESERVE src0_sel:WORD_1
	v_exp_f16_sdwa v191, v175 clamp dst_sel:WORD_1 dst_unused:UNUSED_PRESERVE src0_sel:WORD_1
	s_nop 0
	s_waitcnt lgkmcnt(5)
	v_mfma_f32_32x32x16_f16 v[18:33], v[102:105], v[194:197], v[18:33]
	ds_read_b128 v[34:37], v179 offset:51136
	v_pk_fma_f16 v191, v191, s5, v188 op_sel_hi:[1,0,0]
	s_nop 0
	v_pk_max_f16 v191, v175, v191
	v_pk_fma_f16 v175, v190, s5, v188 op_sel_hi:[1,0,0]
	s_nop 0
	v_pk_max_f16 v190, v174, v175
	s_waitcnt lgkmcnt(5)
	v_mfma_f32_32x32x16_f16 v[18:33], v[74:77], v[202:205], v[18:33]
	ds_read_b128 v[194:197], v179 offset:51168
	v_cvt_pk_f16_f32 v46, v46, v47
	v_cvt_pk_f16_f32 v47, v48, v49
	s_waitcnt lgkmcnt(5)
	v_mfma_f32_32x32x16_f16 v[18:33], v[106:109], v[38:41], v[18:33]
	v_exp_f16_e64 v48, v46 clamp
	v_exp_f16_e64 v49, v47 clamp
	v_exp_f16_sdwa v48, v46 clamp dst_sel:WORD_1 dst_unused:UNUSED_PRESERVE src0_sel:WORD_1
	v_exp_f16_sdwa v49, v47 clamp dst_sel:WORD_1 dst_unused:UNUSED_PRESERVE src0_sel:WORD_1
	s_nop 0
	s_waitcnt lgkmcnt(4)
	v_mfma_f32_32x32x16_f16 v[18:33], v[82:85], v[180:183], v[18:33]
	v_pk_fma_f16 v38, v49, s5, v188 op_sel_hi:[1,0,0]
	s_nop 0
	v_pk_max_f16 v193, v47, v38
	v_pk_fma_f16 v38, v48, s5, v188 op_sel_hi:[1,0,0]
	s_nop 0
	v_pk_max_f16 v192, v46, v38
	s_waitcnt lgkmcnt(3)
	v_mfma_f32_32x32x16_f16 v[18:33], v[110:113], v[184:187], v[18:33]
	s_waitcnt vmcnt(2)
	v_pk_add_f16 v40, v162, v146
	v_pk_add_f16 v41, v163, v147
	s_nop 0
	v_pk_mul_f16 v38, v164, v148 clamp
	v_pk_mul_f16 v39, v165, v149 clamp
	v_pk_max_f16 v38, v40, v38
	v_pk_max_f16 v39, v41, v39
	ds_write_b64 v189, v[38:39] offset:16896
	v_mfma_f32_16x16x32_f16 v[62:65], v[66:69], v[190:193], v[62:65]
	s_waitcnt lgkmcnt(3)
	v_mfma_f32_32x32x16_f16 v[18:33], v[94:97], v[42:45], v[18:33]
	v_pk_add_f16 v40, v162, v138
	v_pk_add_f16 v41, v163, v139
	s_nop 0
	v_pk_mul_f16 v38, v164, v140 clamp
	v_pk_mul_f16 v39, v165, v141 clamp
	v_pk_max_f16 v38, v40, v38
	v_pk_max_f16 v39, v41, v39
	ds_write_b64 v189, v[38:39] offset:17424
	s_waitcnt lgkmcnt(3)
	v_mfma_f32_32x32x16_f16 v[18:33], v[134:137], v[34:37], v[18:33]
	v_pk_add_f16 v40, v162, v150
	v_pk_add_f16 v41, v163, v151
	s_nop 0
	v_pk_mul_f16 v38, v164, v152 clamp
	v_pk_mul_f16 v39, v165, v153 clamp
	v_pk_max_f16 v38, v40, v38
	v_pk_max_f16 v39, v41, v39
	ds_write_b64 v189, v[38:39] offset:17952
	s_waitcnt lgkmcnt(3)
	v_mfma_f32_32x32x16_f16 v[18:33], v[130:133], v[194:197], v[18:33]
	v_pk_add_f16 v36, v162, v142
	v_pk_add_f16 v37, v163, v143
	s_nop 0
	v_pk_mul_f16 v34, v164, v144 clamp
	v_pk_mul_f16 v35, v165, v145 clamp
	v_pk_max_f16 v34, v36, v34
	v_pk_max_f16 v35, v37, v35
	ds_write_b64 v189, v[34:35] offset:18480
	v_mov_b32_e32 v34, 0x14000
	v_lshl_add_u32 v211, v170, 2, v34
	v_mov_b32_e32 v34, 0x14008
	v_lshl_add_u32 v34, v167, 2, v34
	s_mov_b32 s5, 0x14000
	v_add3_u32 v34, v171, v172, s5
	ds_write2_b32 v211, v62, v63 offset1:1
	s_and_saveexec_b64 s[6:7], s[0:1]
	ds_write2_b32 v211, v64, v65 offset0:2 offset1:3
	s_or_b64 exec, exec, s[6:7]
	s_mov_b32 s21, 0
	s_mov_b32 s5, s21
	v_lshl_add_u64 v[168:169], v[168:169], 0, s[4:5]
	s_sub_i32 s4, 0x7e, s28
	s_mul_i32 s4, s4, 6
	s_ashr_i32 s5, s4, 31
	s_add_u32 s26, s8, s4
	s_addc_u32 s27, s9, s5
	s_or_b32 s31, s28, 1
	s_or_b64 s[4:5], s[18:19], s[22:23]
	s_and_b64 s[4:5], s[4:5], exec
	s_cselect_b32 s6, s13, s46
	s_cselect_b32 s7, s12, s45
	s_lshl_b32 s4, s30, 6
	s_ashr_i32 s5, s4, 31
	s_lshl_b64 s[4:5], s[4:5], 4
	s_add_u32 s4, s7, s4
	s_addc_u32 s5, s6, s5
	s_lshl_b32 s51, s29, 4
	s_sub_i32 s9, 0xff, s51
	s_mul_i32 s9, s9, s51
	s_sub_i32 s28, s43, s29
	s_ashr_i32 s9, s9, 1
	s_lshl_b32 s28, s28, 4
	s_add_i32 s9, s28, s9
	s_add_i32 s9, s9, -1
	s_mul_i32 s8, s33, 0x1fc0
	s_ashr_i32 s28, s9, 31
	v_mov_b32_e32 v167, 0
	v_lshlrev_b32_e32 v34, 2, v173
	s_add_u32 s8, s9, s8
	v_lshl_add_u64 v[174:175], s[4:5], 0, v[166:167]
	v_cndmask_b32_e64 v231, 0, 1, s[16:17]
	s_movk_i32 s4, 0xc0
	v_add_u32_e32 v200, 0x12400, v34
	s_addc_u32 s9, s28, 0
	v_add_u32_e32 v190, 0x14000, v34
	v_add_u32_e32 v180, 0x15c00, v34
	v_add_u32_e32 v216, 0x10800, v34
	v_add_u32_e32 v209, 0x125c0, v34
	v_add_u32_e32 v210, 0x12940, v34
	v_add_u32_e32 v207, 0x12cc0, v34
	v_add_u32_e32 v208, 0x13040, v34
	v_add_u32_e32 v204, 0x133c0, v34
	v_add_u32_e32 v205, 0x13740, v34
	v_add_u32_e32 v202, 0x13ac0, v34
	v_add_u32_e32 v203, 0x13e40, v34
	v_add_u32_e32 v197, 0x141c0, v34
	v_add_u32_e32 v198, 0x14540, v34
	v_add_u32_e32 v195, 0x148c0, v34
	v_add_u32_e32 v196, 0x14c40, v34
	v_add_u32_e32 v193, 0x14fc0, v34
	v_add_u32_e32 v194, 0x15340, v34
	v_add_u32_e32 v191, 0x156c0, v34
	v_add_u32_e32 v192, 0x15a40, v34
	v_add_u32_e32 v187, 0x15dc0, v34
	v_add_u32_e32 v188, 0x16140, v34
	v_add_u32_e32 v185, 0x164c0, v34
	v_add_u32_e32 v186, 0x16840, v34
	v_add_u32_e32 v183, 0x16bc0, v34
	v_add_u32_e32 v184, 0x16f40, v34
	v_add_u32_e32 v181, 0x172c0, v34
	v_add_u32_e32 v182, 0x17640, v34
	v_add_u32_e32 v223, 0x109c0, v34
	v_add_u32_e32 v224, 0x10d40, v34
	v_add_u32_e32 v221, 0x110c0, v34
	v_add_u32_e32 v222, 0x11440, v34
	v_add_u32_e32 v219, 0x117c0, v34
	v_add_u32_e32 v220, 0x11b40, v34
	v_add_u32_e32 v217, 0x11ec0, v34
	v_add_u32_e32 v218, 0x12240, v34
	v_mov_b32_e32 v34, 0x17800
	v_cndmask_b32_e64 v230, 0, 1, s[18:19]
	v_readfirstlane_b32 s50, v231
	v_cmp_gt_u32_e64 s[6:7], s4, v0
	s_movk_i32 s4, 0x60
	s_mul_i32 s9, s9, 6
	s_mul_hi_u32 s28, s8, 6
	v_mov_b32_e32 v35, 0x15c00
	v_add_u32_e32 v228, 0x15c00, v171
	v_add_u32_e32 v226, 0x10800, v171
	v_add_u32_e32 v215, 0x12400, v171
	v_add_u32_e32 v213, 0x14000, v171
	v_lshl_add_u32 v232, v177, 2, v34
	v_cndmask_b32_e64 v34, 0, 1, s[24:25]
	s_mov_b32 s48, 1
	v_readfirstlane_b32 s49, v230
	v_cmp_gt_u32_e64 s[4:5], s4, v0
	s_add_i32 s52, s28, s9
	s_mul_i32 s53, s8, 6
	v_lshl_add_u32 v229, v170, 2, v35
	v_add_u32_e32 v227, v228, v172
	v_add_u32_e32 v225, v226, v172
	v_add_u32_e32 v214, v215, v172
	v_add_u32_e32 v212, v213, v172
	s_mov_b32 s56, 8
	s_mov_b32 s54, 16
	v_cmp_ne_u32_e64 s[8:9], 1, v34
	s_movk_i32 s55, 0x3dc5
	v_mov_b32_e32 v233, 0xbdc5
	v_add_u32_e32 v234, 0x700, v200
	v_add_u32_e32 v235, 0xe00, v200
	v_add_u32_e32 v236, 0x1500, v200
	v_add_u32_e32 v237, 0x700, v190
	v_add_u32_e32 v238, 0xe00, v190
	v_add_u32_e32 v239, 0x1500, v190
	s_mov_b32 s41, s50
	s_waitcnt lgkmcnt(0)
	s_barrier
	ds_read_b128 v[50:53], v179
	ds_read_b128 v[54:57], v179 offset:32
	ds_read_b128 v[58:61], v179 offset:64
	s_and_b64 vcc, exec, s[8:9]
	s_cbranch_vccnz .LBB1_50

.LBB1_59:
	global_load_dwordx4 v[162:165], v[168:169], off
	ds_read_b128 v[62:65], v179 offset:96
	ds_read_b128 v[170:173], v179 offset:128
	ds_read_b128 v[240:243], v179 offset:160
	s_waitcnt lgkmcnt(5)
	v_mfma_f32_32x32x16_f16 v[34:49], v[122:125], v[50:53], v[2:17]
	ds_read_b128 v[244:247], v179 offset:192
	v_cvt_pk_f16_f32 v166, v18, v19
	v_cvt_pk_f16_f32 v167, v20, v21
	s_waitcnt lgkmcnt(5)
	v_mfma_f32_32x32x16_f16 v[34:49], v[98:101], v[54:57], v[34:49]
	ds_read_b128 v[18:21], v179 offset:224
	v_exp_f16_e64 v50, v166 clamp
	v_exp_f16_e64 v51, v167 clamp
	v_exp_f16_sdwa v50, v166 clamp dst_sel:WORD_1 dst_unused:UNUSED_PRESERVE src0_sel:WORD_1
	v_exp_f16_sdwa v51, v167 clamp dst_sel:WORD_1 dst_unused:UNUSED_PRESERVE src0_sel:WORD_1
	s_nop 0
	s_waitcnt lgkmcnt(5)
	v_mfma_f32_32x32x16_f16 v[34:49], v[114:117], v[58:61], v[34:49]
	ds_read_b128 v[248:251], v179 offset:256
	v_pk_fma_f16 v51, v51, s55, v233 op_sel_hi:[1,0,0]
	v_pk_fma_f16 v50, v50, s55, v233 op_sel_hi:[1,0,0]
	v_pk_max_f16 v51, v167, v51
	v_pk_max_f16 v50, v166, v50
	s_waitcnt lgkmcnt(5)
	v_mfma_f32_32x32x16_f16 v[34:49], v[86:89], v[62:65], v[34:49]
	ds_read_b128 v[252:255], v179 offset:288
	v_cvt_pk_f16_f32 v52, v22, v23
	v_cvt_pk_f16_f32 v53, v24, v25
	s_waitcnt lgkmcnt(5)
	v_mfma_f32_32x32x16_f16 v[34:49], v[126:129], v[170:173], v[34:49]
	ds_read_b128 v[22:25], v179 offset:320
	v_exp_f16_e64 v54, v52 clamp
	v_exp_f16_e64 v55, v53 clamp
	v_exp_f16_sdwa v54, v52 clamp dst_sel:WORD_1 dst_unused:UNUSED_PRESERVE src0_sel:WORD_1
	v_exp_f16_sdwa v55, v53 clamp dst_sel:WORD_1 dst_unused:UNUSED_PRESERVE src0_sel:WORD_1
	s_nop 0
	s_waitcnt lgkmcnt(5)
	v_mfma_f32_32x32x16_f16 v[34:49], v[90:93], v[240:243], v[34:49]
	ds_read_b128 v[170:173], v179 offset:352
	v_pk_fma_f16 v55, v55, s55, v233 op_sel_hi:[1,0,0]
	v_pk_fma_f16 v54, v54, s55, v233 op_sel_hi:[1,0,0]
	v_pk_max_f16 v53, v53, v55
	v_pk_max_f16 v52, v52, v54
	s_waitcnt lgkmcnt(5)
	v_mfma_f32_32x32x16_f16 v[34:49], v[118:121], v[244:247], v[34:49]
	ds_read_b128 v[240:243], v179 offset:384
	v_cvt_pk_f16_f32 v166, v26, v27
	v_cvt_pk_f16_f32 v167, v28, v29
	v_mfma_f32_16x16x32_f16 v[62:65], v[70:73], v[50:53], 0
	s_waitcnt lgkmcnt(5)
	v_mfma_f32_32x32x16_f16 v[34:49], v[78:81], v[18:21], v[34:49]
	ds_read_b128 v[26:29], v179 offset:416
	v_exp_f16_e64 v244, v166 clamp
	v_exp_f16_e64 v245, v167 clamp
	v_exp_f16_sdwa v244, v166 clamp dst_sel:WORD_1 dst_unused:UNUSED_PRESERVE src0_sel:WORD_1
	v_exp_f16_sdwa v245, v167 clamp dst_sel:WORD_1 dst_unused:UNUSED_PRESERVE src0_sel:WORD_1
	s_nop 0
	s_waitcnt lgkmcnt(5)
	v_mfma_f32_32x32x16_f16 v[34:49], v[102:105], v[248:251], v[34:49]
	ds_read_b128 v[18:21], v179 offset:448
	v_pk_fma_f16 v245, v245, s55, v233 op_sel_hi:[1,0,0]
	s_nop 0
	v_pk_max_f16 v245, v167, v245
	v_pk_fma_f16 v167, v244, s55, v233 op_sel_hi:[1,0,0]
	s_nop 0
	v_pk_max_f16 v244, v166, v167
	s_waitcnt lgkmcnt(5)
	v_mfma_f32_32x32x16_f16 v[34:49], v[74:77], v[252:255], v[34:49]
	ds_read_b128 v[248:251], v179 offset:480
	v_cvt_pk_f16_f32 v30, v30, v31
	v_cvt_pk_f16_f32 v31, v32, v33
	s_waitcnt lgkmcnt(5)
	v_mfma_f32_32x32x16_f16 v[34:49], v[106:109], v[22:25], v[34:49]
	v_exp_f16_e64 v32, v30 clamp
	v_exp_f16_e64 v33, v31 clamp
	v_exp_f16_sdwa v32, v30 clamp dst_sel:WORD_1 dst_unused:UNUSED_PRESERVE src0_sel:WORD_1
	v_exp_f16_sdwa v33, v31 clamp dst_sel:WORD_1 dst_unused:UNUSED_PRESERVE src0_sel:WORD_1
	s_nop 0
	s_waitcnt lgkmcnt(4)
	v_mfma_f32_32x32x16_f16 v[34:49], v[82:85], v[170:173], v[34:49]
	v_pk_fma_f16 v22, v33, s55, v233 op_sel_hi:[1,0,0]
	s_nop 0
	v_pk_max_f16 v247, v31, v22
	v_pk_fma_f16 v22, v32, s55, v233 op_sel_hi:[1,0,0]
	s_nop 0
	v_pk_max_f16 v246, v30, v22
	s_waitcnt lgkmcnt(3)
	v_mfma_f32_32x32x16_f16 v[34:49], v[110:113], v[240:243], v[34:49]
	s_waitcnt vmcnt(2)
	v_pk_add_f16 v24, v154, v146
	v_pk_add_f16 v25, v155, v147
	s_nop 0
	v_pk_mul_f16 v22, v156, v148 clamp
	v_pk_mul_f16 v23, v157, v149 clamp
	v_pk_max_f16 v22, v24, v22
	v_pk_max_f16 v23, v25, v23
	ds_write_b64 v189, v[22:23] offset:33792
	v_mfma_f32_16x16x32_f16 v[62:65], v[66:69], v[244:247], v[62:65]
	s_waitcnt lgkmcnt(3)
	v_mfma_f32_32x32x16_f16 v[34:49], v[94:97], v[26:29], v[34:49]
	v_pk_add_f16 v24, v154, v138
	v_pk_add_f16 v25, v155, v139
	s_nop 0
	v_pk_mul_f16 v22, v156, v140 clamp
	v_pk_mul_f16 v23, v157, v141 clamp
	v_pk_max_f16 v22, v24, v22
	v_pk_max_f16 v23, v25, v23
	ds_write_b64 v189, v[22:23] offset:34320
	s_waitcnt lgkmcnt(3)
	v_mfma_f32_32x32x16_f16 v[34:49], v[134:137], v[18:21], v[34:49]
	v_pk_add_f16 v24, v154, v150
	v_pk_add_f16 v25, v155, v151
	s_nop 0
	v_pk_mul_f16 v22, v156, v152 clamp
	v_pk_mul_f16 v23, v157, v153 clamp
	v_pk_max_f16 v22, v24, v22
	v_pk_max_f16 v23, v25, v23
	ds_write_b64 v189, v[22:23] offset:34848
	s_waitcnt lgkmcnt(3)
	v_mfma_f32_32x32x16_f16 v[34:49], v[130:133], v[248:251], v[34:49]
	v_pk_add_f16 v20, v154, v142
	v_pk_add_f16 v21, v155, v143
	s_nop 0
	v_pk_mul_f16 v18, v156, v144 clamp
	v_pk_mul_f16 v19, v157, v145 clamp
	v_pk_max_f16 v18, v20, v18
	v_pk_max_f16 v19, v21, v19
	ds_write_b64 v189, v[18:19] offset:35376
	ds_write2_b32 v229, v62, v63 offset1:1
	s_and_saveexec_b64 s[28:29], s[0:1]
	ds_write2_b32 v229, v64, v65 offset0:2 offset1:3
	s_or_b64 exec, exec, s[28:29]
	v_lshl_add_u64 v[166:167], s[20:21], 4, v[168:169]
	global_load_dwordx4 v[154:157], v[166:167], off
	ds_read_b128 v[50:53], v179 offset:16896
	ds_read_b128 v[54:57], v179 offset:16928
	ds_read_b128 v[58:61], v179 offset:16960
	ds_read_b128 v[62:65], v179 offset:16992
	ds_read_b128 v[168:171], v179 offset:17024
	ds_read_b128 v[240:243], v179 offset:17056
	s_waitcnt lgkmcnt(5)
	v_mfma_f32_32x32x16_f16 v[18:33], v[122:125], v[50:53], v[2:17]
	ds_read_b128 v[244:247], v179 offset:17088
	v_cvt_pk_f16_f32 v172, v34, v35
	v_cvt_pk_f16_f32 v173, v36, v37
	s_waitcnt lgkmcnt(5)
	v_mfma_f32_32x32x16_f16 v[18:33], v[98:101], v[54:57], v[18:33]
	ds_read_b128 v[34:37], v179 offset:17120
	v_exp_f16_e64 v50, v172 clamp
	v_exp_f16_e64 v51, v173 clamp
	v_exp_f16_sdwa v50, v172 clamp dst_sel:WORD_1 dst_unused:UNUSED_PRESERVE src0_sel:WORD_1
	v_exp_f16_sdwa v51, v173 clamp dst_sel:WORD_1 dst_unused:UNUSED_PRESERVE src0_sel:WORD_1
	s_nop 0
	s_waitcnt lgkmcnt(5)
	v_mfma_f32_32x32x16_f16 v[18:33], v[114:117], v[58:61], v[18:33]
	ds_read_b128 v[248:251], v179 offset:17152
	v_pk_fma_f16 v51, v51, s55, v233 op_sel_hi:[1,0,0]
	v_pk_fma_f16 v50, v50, s55, v233 op_sel_hi:[1,0,0]
	v_pk_max_f16 v51, v173, v51
	v_pk_max_f16 v50, v172, v50
	s_waitcnt lgkmcnt(5)
	v_mfma_f32_32x32x16_f16 v[18:33], v[86:89], v[62:65], v[18:33]
	ds_read_b128 v[252:255], v179 offset:17184
	v_cvt_pk_f16_f32 v52, v38, v39
	v_cvt_pk_f16_f32 v53, v40, v41
	s_waitcnt lgkmcnt(5)
	v_mfma_f32_32x32x16_f16 v[18:33], v[126:129], v[168:171], v[18:33]
	ds_read_b128 v[38:41], v179 offset:17216
	v_exp_f16_e64 v54, v52 clamp
	v_exp_f16_e64 v55, v53 clamp
	v_exp_f16_sdwa v54, v52 clamp dst_sel:WORD_1 dst_unused:UNUSED_PRESERVE src0_sel:WORD_1
	v_exp_f16_sdwa v55, v53 clamp dst_sel:WORD_1 dst_unused:UNUSED_PRESERVE src0_sel:WORD_1
	s_nop 0
	s_waitcnt lgkmcnt(5)
	v_mfma_f32_32x32x16_f16 v[18:33], v[90:93], v[240:243], v[18:33]
	ds_read_b128 v[168:171], v179 offset:17248
	v_pk_fma_f16 v55, v55, s55, v233 op_sel_hi:[1,0,0]
	v_pk_fma_f16 v54, v54, s55, v233 op_sel_hi:[1,0,0]
	v_pk_max_f16 v53, v53, v55
	v_pk_max_f16 v52, v52, v54
	s_waitcnt lgkmcnt(5)
	v_mfma_f32_32x32x16_f16 v[18:33], v[118:121], v[244:247], v[18:33]
	ds_read_b128 v[240:243], v179 offset:17280
	v_cvt_pk_f16_f32 v172, v42, v43
	v_cvt_pk_f16_f32 v173, v44, v45
	v_mfma_f32_16x16x32_f16 v[62:65], v[70:73], v[50:53], 0
	s_waitcnt lgkmcnt(5)
	v_mfma_f32_32x32x16_f16 v[18:33], v[78:81], v[34:37], v[18:33]
	ds_read_b128 v[42:45], v179 offset:17312
	v_exp_f16_e64 v244, v172 clamp
	v_exp_f16_e64 v245, v173 clamp
	v_exp_f16_sdwa v244, v172 clamp dst_sel:WORD_1 dst_unused:UNUSED_PRESERVE src0_sel:WORD_1
	v_exp_f16_sdwa v245, v173 clamp dst_sel:WORD_1 dst_unused:UNUSED_PRESERVE src0_sel:WORD_1
	s_nop 0
	s_waitcnt lgkmcnt(5)
	v_mfma_f32_32x32x16_f16 v[18:33], v[102:105], v[248:251], v[18:33]
	ds_read_b128 v[34:37], v179 offset:17344
	v_pk_fma_f16 v245, v245, s55, v233 op_sel_hi:[1,0,0]
	s_nop 0
	v_pk_max_f16 v245, v173, v245
	v_pk_fma_f16 v173, v244, s55, v233 op_sel_hi:[1,0,0]
	s_nop 0
	v_pk_max_f16 v244, v172, v173
	s_waitcnt lgkmcnt(5)
	v_mfma_f32_32x32x16_f16 v[18:33], v[74:77], v[252:255], v[18:33]
	ds_read_b128 v[248:251], v179 offset:17376
	v_cvt_pk_f16_f32 v46, v46, v47
	v_cvt_pk_f16_f32 v47, v48, v49
	s_waitcnt lgkmcnt(5)
	v_mfma_f32_32x32x16_f16 v[18:33], v[106:109], v[38:41], v[18:33]
	v_exp_f16_e64 v48, v46 clamp
	v_exp_f16_e64 v49, v47 clamp
	v_exp_f16_sdwa v48, v46 clamp dst_sel:WORD_1 dst_unused:UNUSED_PRESERVE src0_sel:WORD_1
	v_exp_f16_sdwa v49, v47 clamp dst_sel:WORD_1 dst_unused:UNUSED_PRESERVE src0_sel:WORD_1
	s_nop 0
	s_waitcnt lgkmcnt(4)
	v_mfma_f32_32x32x16_f16 v[18:33], v[82:85], v[168:171], v[18:33]
	v_pk_fma_f16 v38, v49, s55, v233 op_sel_hi:[1,0,0]
	s_nop 0
	v_pk_max_f16 v247, v47, v38
	v_pk_fma_f16 v38, v48, s55, v233 op_sel_hi:[1,0,0]
	s_nop 0
	v_pk_max_f16 v246, v46, v38
	s_waitcnt lgkmcnt(3)
	v_mfma_f32_32x32x16_f16 v[18:33], v[110:113], v[240:243], v[18:33]
	s_waitcnt vmcnt(2)
	v_pk_add_f16 v40, v158, v146
	v_pk_add_f16 v41, v159, v147
	s_nop 0
	v_pk_mul_f16 v38, v160, v148 clamp
	v_pk_mul_f16 v39, v161, v149 clamp
	v_pk_max_f16 v38, v40, v38
	v_pk_max_f16 v39, v41, v39
	ds_write_b64 v189, v[38:39] offset:50688
	v_mfma_f32_16x16x32_f16 v[62:65], v[66:69], v[244:247], v[62:65]
	s_waitcnt lgkmcnt(3)
	v_mfma_f32_32x32x16_f16 v[18:33], v[94:97], v[42:45], v[18:33]
	v_pk_add_f16 v40, v158, v138
	v_pk_add_f16 v41, v159, v139
	s_nop 0
	v_pk_mul_f16 v38, v160, v140 clamp
	v_pk_mul_f16 v39, v161, v141 clamp
	v_pk_max_f16 v38, v40, v38
	v_pk_max_f16 v39, v41, v39
	ds_write_b64 v189, v[38:39] offset:51216
	s_waitcnt lgkmcnt(3)
	v_mfma_f32_32x32x16_f16 v[18:33], v[134:137], v[34:37], v[18:33]
	v_pk_add_f16 v40, v158, v150
	v_pk_add_f16 v41, v159, v151
	s_nop 0
	v_pk_mul_f16 v38, v160, v152 clamp
	v_pk_mul_f16 v39, v161, v153 clamp
	v_pk_max_f16 v38, v40, v38
	v_pk_max_f16 v39, v41, v39
	ds_write_b64 v189, v[38:39] offset:51744
	s_waitcnt lgkmcnt(3)
	v_mfma_f32_32x32x16_f16 v[18:33], v[130:133], v[248:251], v[18:33]
	v_pk_add_f16 v36, v158, v142
	v_pk_add_f16 v37, v159, v143
	s_nop 0
	v_pk_mul_f16 v34, v160, v144 clamp
	v_pk_mul_f16 v35, v161, v145 clamp
	v_pk_max_f16 v34, v36, v34
	v_pk_max_f16 v35, v37, v35
	ds_write_b64 v189, v[34:35] offset:52272
	ds_write2_b32 v206, v62, v63 offset1:1
	s_and_saveexec_b64 s[28:29], s[0:1]
	ds_write2_b32 v206, v64, v65 offset0:2 offset1:3
	s_or_b64 exec, exec, s[28:29]
	s_sub_i32 s28, 0x7d, s31
	s_mul_i32 s28, s28, 6
	s_ashr_i32 s29, s28, 31
	s_add_u32 s26, s26, s28
	s_addc_u32 s27, s27, s29
	s_and_b64 vcc, exec, s[8:9]
	s_waitcnt lgkmcnt(0)
	s_barrier
	ds_read_b128 v[50:53], v179 offset:33792
	ds_read_b128 v[54:57], v179 offset:33824
	ds_read_b128 v[58:61], v179 offset:33856
	s_cbranch_vccnz .LBB1_76
	s_cmp_lg_u32 s41, 0
	s_cbranch_scc0 .LBB1_72
	s_and_saveexec_b64 s[28:29], s[6:7]
	s_cbranch_execz .LBB1_71
	ds_read2_b32 v[34:35], v180 offset1:224
	v_add_u32_e32 v36, 0x700, v180
	ds_read2_b32 v[36:37], v36 offset1:224
	v_add_u32_e32 v38, 0xe00, v180
	s_lshl_b32 s30, s56, 28
	s_waitcnt lgkmcnt(1)
	v_add_f32_e32 v34, 0, v34
	v_add_f32_e32 v40, v34, v35
	ds_read2_b32 v[34:35], v38 offset1:224
	v_add_u32_e32 v38, 0x1500, v180
	ds_read2_b32 v[38:39], v38 offset1:224
	s_waitcnt lgkmcnt(2)
	v_add_f32_e32 v36, v40, v36
	v_add_f32_e32 v36, v36, v37
	s_waitcnt lgkmcnt(1)
	v_add_f32_e32 v34, v36, v34
	s_add_i32 s30, s30, 0xb0000000
	v_add_f32_e32 v34, v34, v35
	s_ashr_i32 s30, s30, 31
	s_waitcnt lgkmcnt(0)
	v_add_f32_e32 v34, v34, v38
	s_and_b32 s30, s30, 0x1800
	v_add_f32_e32 v34, v34, v39
	v_add_u32_e32 v35, s30, v232
	ds_write_b32 v35, v34 offset:384

.LBB1_93:
	v_lshl_add_u64 v[158:159], s[20:21], 4, v[166:167]
	global_load_dwordx4 v[170:173], v[158:159], off
	ds_read_b128 v[62:65], v179 offset:33888
	ds_read_b128 v[166:169], v179 offset:33920
	ds_read_b128 v[240:243], v179 offset:33952
	s_add_i32 s34, s57, 1
	s_waitcnt lgkmcnt(5)
	v_mfma_f32_32x32x16_f16 v[34:49], v[122:125], v[50:53], v[2:17]
	ds_read_b128 v[244:247], v179 offset:33984
	v_cvt_pk_f16_f32 v160, v18, v19
	v_cvt_pk_f16_f32 v161, v20, v21
	s_waitcnt lgkmcnt(5)
	v_mfma_f32_32x32x16_f16 v[34:49], v[98:101], v[54:57], v[34:49]
	ds_read_b128 v[18:21], v179 offset:34016
	v_exp_f16_e64 v50, v160 clamp
	v_exp_f16_e64 v51, v161 clamp
	v_exp_f16_sdwa v50, v160 clamp dst_sel:WORD_1 dst_unused:UNUSED_PRESERVE src0_sel:WORD_1
	v_exp_f16_sdwa v51, v161 clamp dst_sel:WORD_1 dst_unused:UNUSED_PRESERVE src0_sel:WORD_1
	s_nop 0
	s_waitcnt lgkmcnt(5)
	v_mfma_f32_32x32x16_f16 v[34:49], v[114:117], v[58:61], v[34:49]
	ds_read_b128 v[248:251], v179 offset:34048
	v_pk_fma_f16 v51, v51, s55, v233 op_sel_hi:[1,0,0]
	v_pk_fma_f16 v50, v50, s55, v233 op_sel_hi:[1,0,0]
	v_pk_max_f16 v51, v161, v51
	v_pk_max_f16 v50, v160, v50
	s_waitcnt lgkmcnt(5)
	v_mfma_f32_32x32x16_f16 v[34:49], v[86:89], v[62:65], v[34:49]
	ds_read_b128 v[252:255], v179 offset:34080
	v_cvt_pk_f16_f32 v52, v22, v23
	v_cvt_pk_f16_f32 v53, v24, v25
	s_waitcnt lgkmcnt(5)
	v_mfma_f32_32x32x16_f16 v[34:49], v[126:129], v[166:169], v[34:49]
	ds_read_b128 v[22:25], v179 offset:34112
	v_exp_f16_e64 v54, v52 clamp
	v_exp_f16_e64 v55, v53 clamp
	v_exp_f16_sdwa v54, v52 clamp dst_sel:WORD_1 dst_unused:UNUSED_PRESERVE src0_sel:WORD_1
	v_exp_f16_sdwa v55, v53 clamp dst_sel:WORD_1 dst_unused:UNUSED_PRESERVE src0_sel:WORD_1
	s_nop 0
	s_waitcnt lgkmcnt(5)
	v_mfma_f32_32x32x16_f16 v[34:49], v[90:93], v[240:243], v[34:49]
	ds_read_b128 v[166:169], v179 offset:34144
	v_pk_fma_f16 v55, v55, s55, v233 op_sel_hi:[1,0,0]
	v_pk_fma_f16 v54, v54, s55, v233 op_sel_hi:[1,0,0]
	v_pk_max_f16 v53, v53, v55
	v_pk_max_f16 v52, v52, v54
	s_waitcnt lgkmcnt(5)
	v_mfma_f32_32x32x16_f16 v[34:49], v[118:121], v[244:247], v[34:49]
	ds_read_b128 v[240:243], v179 offset:34176
	v_cvt_pk_f16_f32 v160, v26, v27
	v_cvt_pk_f16_f32 v161, v28, v29
	v_mfma_f32_16x16x32_f16 v[62:65], v[70:73], v[50:53], 0
	s_waitcnt lgkmcnt(5)
	v_mfma_f32_32x32x16_f16 v[34:49], v[78:81], v[18:21], v[34:49]
	ds_read_b128 v[26:29], v179 offset:34208
	v_exp_f16_e64 v244, v160 clamp
	v_exp_f16_e64 v245, v161 clamp
	v_exp_f16_sdwa v244, v160 clamp dst_sel:WORD_1 dst_unused:UNUSED_PRESERVE src0_sel:WORD_1
	v_exp_f16_sdwa v245, v161 clamp dst_sel:WORD_1 dst_unused:UNUSED_PRESERVE src0_sel:WORD_1
	s_nop 0
	s_waitcnt lgkmcnt(5)
	v_mfma_f32_32x32x16_f16 v[34:49], v[102:105], v[248:251], v[34:49]
	ds_read_b128 v[18:21], v179 offset:34240
	v_pk_fma_f16 v245, v245, s55, v233 op_sel_hi:[1,0,0]
	s_nop 0
	v_pk_max_f16 v245, v161, v245
	v_pk_fma_f16 v161, v244, s55, v233 op_sel_hi:[1,0,0]
	s_nop 0
	v_pk_max_f16 v244, v160, v161
	s_waitcnt lgkmcnt(5)
	v_mfma_f32_32x32x16_f16 v[34:49], v[74:77], v[252:255], v[34:49]
	ds_read_b128 v[248:251], v179 offset:34272
	v_cvt_pk_f16_f32 v30, v30, v31
	v_cvt_pk_f16_f32 v31, v32, v33
	s_waitcnt lgkmcnt(5)
	v_mfma_f32_32x32x16_f16 v[34:49], v[106:109], v[22:25], v[34:49]
	v_exp_f16_e64 v32, v30 clamp
	v_exp_f16_e64 v33, v31 clamp
	v_exp_f16_sdwa v32, v30 clamp dst_sel:WORD_1 dst_unused:UNUSED_PRESERVE src0_sel:WORD_1
	v_exp_f16_sdwa v33, v31 clamp dst_sel:WORD_1 dst_unused:UNUSED_PRESERVE src0_sel:WORD_1
	s_nop 0
	s_waitcnt lgkmcnt(4)
	v_mfma_f32_32x32x16_f16 v[34:49], v[82:85], v[166:169], v[34:49]
	v_pk_fma_f16 v22, v33, s55, v233 op_sel_hi:[1,0,0]
	s_nop 0
	v_pk_max_f16 v247, v31, v22
	v_pk_fma_f16 v22, v32, s55, v233 op_sel_hi:[1,0,0]
	s_nop 0
	v_pk_max_f16 v246, v30, v22
	s_waitcnt lgkmcnt(3)
	v_mfma_f32_32x32x16_f16 v[34:49], v[110:113], v[240:243], v[34:49]
	s_waitcnt vmcnt(2)
	v_pk_add_f16 v24, v146, v162
	v_pk_add_f16 v25, v147, v163
	s_nop 0
	v_pk_mul_f16 v22, v164, v148 clamp
	v_pk_mul_f16 v23, v165, v149 clamp
	v_pk_max_f16 v22, v24, v22
	v_pk_max_f16 v23, v25, v23
	ds_write_b64 v189, v[22:23]
	v_mfma_f32_16x16x32_f16 v[62:65], v[66:69], v[244:247], v[62:65]
	s_waitcnt lgkmcnt(3)
	v_mfma_f32_32x32x16_f16 v[34:49], v[94:97], v[26:29], v[34:49]
	v_pk_add_f16 v24, v138, v162
	v_pk_add_f16 v25, v139, v163
	s_nop 0
	v_pk_mul_f16 v22, v164, v140 clamp
	v_pk_mul_f16 v23, v165, v141 clamp
	v_pk_max_f16 v22, v24, v22
	v_pk_max_f16 v23, v25, v23
	ds_write_b64 v189, v[22:23] offset:528
	s_waitcnt lgkmcnt(3)
	v_mfma_f32_32x32x16_f16 v[34:49], v[134:137], v[18:21], v[34:49]
	v_pk_add_f16 v24, v150, v162
	v_pk_add_f16 v25, v151, v163
	s_nop 0
	v_pk_mul_f16 v22, v164, v152 clamp
	v_pk_mul_f16 v23, v165, v153 clamp
	v_pk_max_f16 v22, v24, v22
	v_pk_max_f16 v23, v25, v23
	ds_write_b64 v189, v[22:23] offset:1056
	s_waitcnt lgkmcnt(3)
	v_mfma_f32_32x32x16_f16 v[34:49], v[130:133], v[248:251], v[34:49]
	s_waitcnt vmcnt(1)
	v_pk_add_f16 v20, v142, v162
	v_pk_add_f16 v21, v143, v163
	s_nop 0
	v_pk_mul_f16 v18, v164, v144 clamp
	v_pk_mul_f16 v19, v165, v145 clamp
	v_pk_max_f16 v18, v20, v18
	v_pk_max_f16 v19, v21, v19
	ds_write_b64 v189, v[18:19] offset:1584
	ds_write2_b32 v201, v62, v63 offset1:1
	s_and_saveexec_b64 s[30:31], s[0:1]
	ds_write2_b32 v201, v64, v65 offset0:2 offset1:3
	s_or_b64 exec, exec, s[30:31]
	v_lshl_add_u64 v[158:159], s[20:21], 4, v[158:159]
	global_load_dwordx4 v[166:169], v[158:159], off
	ds_read_b128 v[50:53], v179 offset:50688
	ds_read_b128 v[54:57], v179 offset:50720
	ds_read_b128 v[58:61], v179 offset:50752
	ds_read_b128 v[62:65], v179 offset:50784
	ds_read_b128 v[160:163], v179 offset:50816
	ds_read_b128 v[240:243], v179 offset:50848
	s_waitcnt lgkmcnt(5)
	v_mfma_f32_32x32x16_f16 v[18:33], v[122:125], v[50:53], v[2:17]
	ds_read_b128 v[244:247], v179 offset:50880
	v_cvt_pk_f16_f32 v164, v34, v35
	v_cvt_pk_f16_f32 v165, v36, v37
	s_waitcnt lgkmcnt(5)
	v_mfma_f32_32x32x16_f16 v[18:33], v[98:101], v[54:57], v[18:33]
	ds_read_b128 v[34:37], v179 offset:50912
	v_exp_f16_e64 v50, v164 clamp
	v_exp_f16_e64 v51, v165 clamp
	v_exp_f16_sdwa v50, v164 clamp dst_sel:WORD_1 dst_unused:UNUSED_PRESERVE src0_sel:WORD_1
	v_exp_f16_sdwa v51, v165 clamp dst_sel:WORD_1 dst_unused:UNUSED_PRESERVE src0_sel:WORD_1
	s_nop 0
	s_waitcnt lgkmcnt(5)
	v_mfma_f32_32x32x16_f16 v[18:33], v[114:117], v[58:61], v[18:33]
	ds_read_b128 v[248:251], v179 offset:50944
	v_pk_fma_f16 v51, v51, s55, v233 op_sel_hi:[1,0,0]
	v_pk_fma_f16 v50, v50, s55, v233 op_sel_hi:[1,0,0]
	v_pk_max_f16 v51, v165, v51
	v_pk_max_f16 v50, v164, v50
	s_waitcnt lgkmcnt(5)
	v_mfma_f32_32x32x16_f16 v[18:33], v[86:89], v[62:65], v[18:33]
	ds_read_b128 v[252:255], v179 offset:50976
	v_cvt_pk_f16_f32 v52, v38, v39
	v_cvt_pk_f16_f32 v53, v40, v41
	s_waitcnt lgkmcnt(5)
	v_mfma_f32_32x32x16_f16 v[18:33], v[126:129], v[160:163], v[18:33]
	ds_read_b128 v[38:41], v179 offset:51008
	v_exp_f16_e64 v54, v52 clamp
	v_exp_f16_e64 v55, v53 clamp
	v_exp_f16_sdwa v54, v52 clamp dst_sel:WORD_1 dst_unused:UNUSED_PRESERVE src0_sel:WORD_1
	v_exp_f16_sdwa v55, v53 clamp dst_sel:WORD_1 dst_unused:UNUSED_PRESERVE src0_sel:WORD_1
	s_nop 0
	s_waitcnt lgkmcnt(5)
	v_mfma_f32_32x32x16_f16 v[18:33], v[90:93], v[240:243], v[18:33]
	ds_read_b128 v[160:163], v179 offset:51040
	v_pk_fma_f16 v55, v55, s55, v233 op_sel_hi:[1,0,0]
	v_pk_fma_f16 v54, v54, s55, v233 op_sel_hi:[1,0,0]
	v_pk_max_f16 v53, v53, v55
	v_pk_max_f16 v52, v52, v54
	s_waitcnt lgkmcnt(5)
	v_mfma_f32_32x32x16_f16 v[18:33], v[118:121], v[244:247], v[18:33]
	ds_read_b128 v[240:243], v179 offset:51072
	v_cvt_pk_f16_f32 v164, v42, v43
	v_cvt_pk_f16_f32 v165, v44, v45
	v_mfma_f32_16x16x32_f16 v[62:65], v[70:73], v[50:53], 0
	s_waitcnt lgkmcnt(5)
	v_mfma_f32_32x32x16_f16 v[18:33], v[78:81], v[34:37], v[18:33]
	ds_read_b128 v[42:45], v179 offset:51104
	v_exp_f16_e64 v244, v164 clamp
	v_exp_f16_e64 v245, v165 clamp
	v_exp_f16_sdwa v244, v164 clamp dst_sel:WORD_1 dst_unused:UNUSED_PRESERVE src0_sel:WORD_1
	v_exp_f16_sdwa v245, v165 clamp dst_sel:WORD_1 dst_unused:UNUSED_PRESERVE src0_sel:WORD_1
	s_nop 0
	s_waitcnt lgkmcnt(5)
	v_mfma_f32_32x32x16_f16 v[18:33], v[102:105], v[248:251], v[18:33]
	ds_read_b128 v[34:37], v179 offset:51136
	v_pk_fma_f16 v245, v245, s55, v233 op_sel_hi:[1,0,0]
	s_nop 0
	v_pk_max_f16 v245, v165, v245
	v_pk_fma_f16 v165, v244, s55, v233 op_sel_hi:[1,0,0]
	s_nop 0
	v_pk_max_f16 v244, v164, v165
	s_waitcnt lgkmcnt(5)
	v_mfma_f32_32x32x16_f16 v[18:33], v[74:77], v[252:255], v[18:33]
	ds_read_b128 v[248:251], v179 offset:51168
	v_cvt_pk_f16_f32 v46, v46, v47
	v_cvt_pk_f16_f32 v47, v48, v49
	s_waitcnt lgkmcnt(5)
	v_mfma_f32_32x32x16_f16 v[18:33], v[106:109], v[38:41], v[18:33]
	v_exp_f16_e64 v48, v46 clamp
	v_exp_f16_e64 v49, v47 clamp
	v_exp_f16_sdwa v48, v46 clamp dst_sel:WORD_1 dst_unused:UNUSED_PRESERVE src0_sel:WORD_1
	v_exp_f16_sdwa v49, v47 clamp dst_sel:WORD_1 dst_unused:UNUSED_PRESERVE src0_sel:WORD_1
	s_nop 0
	s_waitcnt lgkmcnt(4)
	v_mfma_f32_32x32x16_f16 v[18:33], v[82:85], v[160:163], v[18:33]
	v_pk_fma_f16 v38, v49, s55, v233 op_sel_hi:[1,0,0]
	s_nop 0
	v_pk_max_f16 v247, v47, v38
	v_pk_fma_f16 v38, v48, s55, v233 op_sel_hi:[1,0,0]
	s_nop 0
	v_pk_max_f16 v246, v46, v38
	s_waitcnt lgkmcnt(3)
	v_mfma_f32_32x32x16_f16 v[18:33], v[110:113], v[240:243], v[18:33]
	v_pk_add_f16 v40, v146, v154
	v_pk_add_f16 v41, v147, v155
	s_nop 0
	v_pk_mul_f16 v38, v156, v148 clamp
	v_pk_mul_f16 v39, v157, v149 clamp
	v_pk_max_f16 v38, v40, v38
	v_pk_max_f16 v39, v41, v39
	ds_write_b64 v189, v[38:39] offset:16896
	v_mfma_f32_16x16x32_f16 v[62:65], v[66:69], v[244:247], v[62:65]
	s_waitcnt lgkmcnt(3)
	v_mfma_f32_32x32x16_f16 v[18:33], v[94:97], v[42:45], v[18:33]
	v_pk_add_f16 v40, v138, v154
	v_pk_add_f16 v41, v139, v155
	s_nop 0
	v_pk_mul_f16 v38, v156, v140 clamp
	v_pk_mul_f16 v39, v157, v141 clamp
	v_pk_max_f16 v38, v40, v38
	v_pk_max_f16 v39, v41, v39
	ds_write_b64 v189, v[38:39] offset:17424
	s_waitcnt lgkmcnt(3)
	v_mfma_f32_32x32x16_f16 v[18:33], v[134:137], v[34:37], v[18:33]
	v_pk_add_f16 v40, v150, v154
	v_pk_add_f16 v41, v151, v155
	s_nop 0
	v_pk_mul_f16 v38, v156, v152 clamp
	v_pk_mul_f16 v39, v157, v153 clamp
	v_pk_max_f16 v38, v40, v38
	v_pk_max_f16 v39, v41, v39
	ds_write_b64 v189, v[38:39] offset:17952
	s_waitcnt lgkmcnt(3)
	v_mfma_f32_32x32x16_f16 v[18:33], v[130:133], v[248:251], v[18:33]
	v_pk_add_f16 v36, v142, v154
	v_pk_add_f16 v37, v143, v155
	s_nop 0
	v_pk_mul_f16 v34, v156, v144 clamp
	v_pk_mul_f16 v35, v157, v145 clamp
	v_pk_max_f16 v34, v36, v34
	v_pk_max_f16 v35, v37, v35
	ds_write_b64 v189, v[34:35] offset:18480
	ds_write2_b32 v211, v62, v63 offset1:1
	s_and_saveexec_b64 s[30:31], s[0:1]
	ds_write2_b32 v211, v64, v65 offset0:2 offset1:3
	s_or_b64 exec, exec, s[30:31]
	s_sub_i32 s30, 0x7d, s34
	s_mul_i32 s30, s30, 6
	s_ashr_i32 s31, s30, 31
	s_add_u32 s28, s28, s30
	s_addc_u32 s29, s29, s31
	s_and_b64 vcc, exec, s[8:9]
	s_waitcnt lgkmcnt(0)
	s_barrier
	ds_read_b128 v[50:53], v179
	ds_read_b128 v[54:57], v179 offset:32
	ds_read_b128 v[58:61], v179 offset:64
	s_cbranch_vccnz .LBB1_110
	s_cmp_eq_u32 s41, 0
	s_cbranch_scc1 .LBB1_106
	s_and_saveexec_b64 s[30:31], s[6:7]
	s_cbranch_execz .LBB1_105
	ds_read2_b32 v[34:35], v200 offset1:224
	ds_read2_b32 v[36:37], v234 offset1:224
	ds_read2_b32 v[38:39], v235 offset1:224
	ds_read2_b32 v[40:41], v236 offset1:224
	s_lshl_b32 s35, s56, 28
	s_add_i32 s35, s35, 0xd0000000
	s_ashr_i32 s35, s35, 31
	s_waitcnt lgkmcnt(3)
	v_add_f32_e32 v34, 0, v34
	v_add_f32_e32 v34, v34, v35
	s_waitcnt lgkmcnt(2)
	v_add_f32_e32 v34, v34, v36
	v_add_f32_e32 v34, v34, v37
	s_waitcnt lgkmcnt(1)
	v_add_f32_e32 v34, v34, v38
	v_add_f32_e32 v34, v34, v39
	s_waitcnt lgkmcnt(0)
	v_add_f32_e32 v34, v34, v40
	s_and_b32 s35, s35, 0x1800
	v_add_f32_e32 v34, v34, v41
	v_add_u32_e32 v35, s35, v232
	ds_write_b32 v35, v34 offset:640

.LBB1_119:
	v_lshl_add_u64 v[154:155], s[20:21], 4, v[158:159]
	global_load_dwordx4 v[158:161], v[154:155], off
	ds_read_b128 v[62:65], v179 offset:96
	ds_read_b128 v[162:165], v179 offset:128
	ds_read_b128 v[240:243], v179 offset:160
	s_waitcnt lgkmcnt(5)
	v_mfma_f32_32x32x16_f16 v[34:49], v[122:125], v[50:53], v[2:17]
	ds_read_b128 v[244:247], v179 offset:192
	v_cvt_pk_f16_f32 v156, v18, v19
	v_cvt_pk_f16_f32 v157, v20, v21
	s_waitcnt lgkmcnt(5)
	v_mfma_f32_32x32x16_f16 v[34:49], v[98:101], v[54:57], v[34:49]
	ds_read_b128 v[18:21], v179 offset:224
	v_exp_f16_e64 v50, v156 clamp
	v_exp_f16_e64 v51, v157 clamp
	v_exp_f16_sdwa v50, v156 clamp dst_sel:WORD_1 dst_unused:UNUSED_PRESERVE src0_sel:WORD_1
	v_exp_f16_sdwa v51, v157 clamp dst_sel:WORD_1 dst_unused:UNUSED_PRESERVE src0_sel:WORD_1
	s_nop 0
	s_waitcnt lgkmcnt(5)
	v_mfma_f32_32x32x16_f16 v[34:49], v[114:117], v[58:61], v[34:49]
	ds_read_b128 v[248:251], v179 offset:256
	v_pk_fma_f16 v51, v51, s55, v233 op_sel_hi:[1,0,0]
	v_pk_fma_f16 v50, v50, s55, v233 op_sel_hi:[1,0,0]
	v_pk_max_f16 v51, v157, v51
	v_pk_max_f16 v50, v156, v50
	s_waitcnt lgkmcnt(5)
	v_mfma_f32_32x32x16_f16 v[34:49], v[86:89], v[62:65], v[34:49]
	ds_read_b128 v[252:255], v179 offset:288
	v_cvt_pk_f16_f32 v52, v22, v23
	v_cvt_pk_f16_f32 v53, v24, v25
	s_waitcnt lgkmcnt(5)
	v_mfma_f32_32x32x16_f16 v[34:49], v[126:129], v[162:165], v[34:49]
	ds_read_b128 v[22:25], v179 offset:320
	v_exp_f16_e64 v54, v52 clamp
	v_exp_f16_e64 v55, v53 clamp
	v_exp_f16_sdwa v54, v52 clamp dst_sel:WORD_1 dst_unused:UNUSED_PRESERVE src0_sel:WORD_1
	v_exp_f16_sdwa v55, v53 clamp dst_sel:WORD_1 dst_unused:UNUSED_PRESERVE src0_sel:WORD_1
	s_nop 0
	s_waitcnt lgkmcnt(5)
	v_mfma_f32_32x32x16_f16 v[34:49], v[90:93], v[240:243], v[34:49]
	ds_read_b128 v[162:165], v179 offset:352
	v_pk_fma_f16 v55, v55, s55, v233 op_sel_hi:[1,0,0]
	v_pk_fma_f16 v54, v54, s55, v233 op_sel_hi:[1,0,0]
	v_pk_max_f16 v53, v53, v55
	v_pk_max_f16 v52, v52, v54
	s_waitcnt lgkmcnt(5)
	v_mfma_f32_32x32x16_f16 v[34:49], v[118:121], v[244:247], v[34:49]
	ds_read_b128 v[240:243], v179 offset:384
	v_cvt_pk_f16_f32 v156, v26, v27
	v_cvt_pk_f16_f32 v157, v28, v29
	v_mfma_f32_16x16x32_f16 v[62:65], v[70:73], v[50:53], 0
	s_waitcnt lgkmcnt(5)
	v_mfma_f32_32x32x16_f16 v[34:49], v[78:81], v[18:21], v[34:49]
	ds_read_b128 v[26:29], v179 offset:416
	v_exp_f16_e64 v244, v156 clamp
	v_exp_f16_e64 v245, v157 clamp
	v_exp_f16_sdwa v244, v156 clamp dst_sel:WORD_1 dst_unused:UNUSED_PRESERVE src0_sel:WORD_1
	v_exp_f16_sdwa v245, v157 clamp dst_sel:WORD_1 dst_unused:UNUSED_PRESERVE src0_sel:WORD_1
	s_nop 0
	s_waitcnt lgkmcnt(5)
	v_mfma_f32_32x32x16_f16 v[34:49], v[102:105], v[248:251], v[34:49]
	ds_read_b128 v[18:21], v179 offset:448
	v_pk_fma_f16 v245, v245, s55, v233 op_sel_hi:[1,0,0]
	s_nop 0
	v_pk_max_f16 v245, v157, v245
	v_pk_fma_f16 v157, v244, s55, v233 op_sel_hi:[1,0,0]
	s_nop 0
	v_pk_max_f16 v244, v156, v157
	s_waitcnt lgkmcnt(5)
	v_mfma_f32_32x32x16_f16 v[34:49], v[74:77], v[252:255], v[34:49]
	ds_read_b128 v[248:251], v179 offset:480
	v_cvt_pk_f16_f32 v30, v30, v31
	v_cvt_pk_f16_f32 v31, v32, v33
	s_waitcnt lgkmcnt(5)
	v_mfma_f32_32x32x16_f16 v[34:49], v[106:109], v[22:25], v[34:49]
	v_exp_f16_e64 v32, v30 clamp
	v_exp_f16_e64 v33, v31 clamp
	v_exp_f16_sdwa v32, v30 clamp dst_sel:WORD_1 dst_unused:UNUSED_PRESERVE src0_sel:WORD_1
	v_exp_f16_sdwa v33, v31 clamp dst_sel:WORD_1 dst_unused:UNUSED_PRESERVE src0_sel:WORD_1
	s_nop 0
	s_waitcnt lgkmcnt(4)
	v_mfma_f32_32x32x16_f16 v[34:49], v[82:85], v[162:165], v[34:49]
	v_pk_fma_f16 v22, v33, s55, v233 op_sel_hi:[1,0,0]
	s_nop 0
	v_pk_max_f16 v247, v31, v22
	v_pk_fma_f16 v22, v32, s55, v233 op_sel_hi:[1,0,0]
	s_nop 0
	v_pk_max_f16 v246, v30, v22
	s_waitcnt lgkmcnt(3)
	v_mfma_f32_32x32x16_f16 v[34:49], v[110:113], v[240:243], v[34:49]
	s_waitcnt vmcnt(2)
	v_pk_add_f16 v24, v170, v146
	v_pk_add_f16 v25, v171, v147
	s_nop 0
	v_pk_mul_f16 v22, v172, v148 clamp
	v_pk_mul_f16 v23, v173, v149 clamp
	v_pk_max_f16 v22, v24, v22
	v_pk_max_f16 v23, v25, v23
	ds_write_b64 v189, v[22:23] offset:33792
	v_mfma_f32_16x16x32_f16 v[62:65], v[66:69], v[244:247], v[62:65]
	s_waitcnt lgkmcnt(3)
	v_mfma_f32_32x32x16_f16 v[34:49], v[94:97], v[26:29], v[34:49]
	v_pk_add_f16 v24, v170, v138
	v_pk_add_f16 v25, v171, v139
	s_nop 0
	v_pk_mul_f16 v22, v172, v140 clamp
	v_pk_mul_f16 v23, v173, v141 clamp
	v_pk_max_f16 v22, v24, v22
	v_pk_max_f16 v23, v25, v23
	ds_write_b64 v189, v[22:23] offset:34320
	s_waitcnt lgkmcnt(3)
	v_mfma_f32_32x32x16_f16 v[34:49], v[134:137], v[18:21], v[34:49]
	v_pk_add_f16 v24, v170, v150
	v_pk_add_f16 v25, v171, v151
	s_nop 0
	v_pk_mul_f16 v22, v172, v152 clamp
	v_pk_mul_f16 v23, v173, v153 clamp
	v_pk_max_f16 v22, v24, v22
	v_pk_max_f16 v23, v25, v23
	ds_write_b64 v189, v[22:23] offset:34848
	s_waitcnt lgkmcnt(3)
	v_mfma_f32_32x32x16_f16 v[34:49], v[130:133], v[248:251], v[34:49]
	v_pk_add_f16 v20, v170, v142
	v_pk_add_f16 v21, v171, v143
	s_nop 0
	v_pk_mul_f16 v18, v172, v144 clamp
	v_pk_mul_f16 v19, v173, v145 clamp
	v_pk_max_f16 v18, v20, v18
	v_pk_max_f16 v19, v21, v19
	ds_write_b64 v189, v[18:19] offset:35376
	ds_write2_b32 v229, v62, v63 offset1:1
	s_and_saveexec_b64 s[30:31], s[0:1]
	ds_write2_b32 v229, v64, v65 offset0:2 offset1:3
	s_or_b64 exec, exec, s[30:31]
	s_cmp_eq_u32 s56, 16
	s_cbranch_scc0 .Lw2_sw_skip
	s_and_b64 vcc, exec, s[16:17]
	s_cbranch_vccz .Lw2_sw_skip
	v_mov_b32_dpp v70, v70 row_shl:8 row_mask:0xa bank_mask:0x3
	v_mov_b32_dpp v71, v71 row_shl:8 row_mask:0xa bank_mask:0x3
	v_mov_b32_dpp v72, v72 row_shl:8 row_mask:0xa bank_mask:0x3
	v_mov_b32_dpp v73, v73 row_shl:8 row_mask:0xa bank_mask:0x3
	v_mov_b32_dpp v66, v66 row_shl:8 row_mask:0xa bank_mask:0x3
	v_mov_b32_dpp v67, v67 row_shl:8 row_mask:0xa bank_mask:0x3
	v_mov_b32_dpp v68, v68 row_shl:8 row_mask:0xa bank_mask:0x3
	v_mov_b32_dpp v69, v69 row_shl:8 row_mask:0xa bank_mask:0x3
.Lw2_sw_skip:
	v_lshl_add_u64 v[154:155], s[20:21], 4, v[154:155]
	global_load_dwordx4 v[162:165], v[154:155], off
	ds_read_b128 v[50:53], v179 offset:16896
	ds_read_b128 v[54:57], v179 offset:16928
	ds_read_b128 v[58:61], v179 offset:16960
	ds_read_b128 v[62:65], v179 offset:16992
	ds_read_b128 v[170:173], v179 offset:17024
	ds_read_b128 v[240:243], v179 offset:17056
	s_waitcnt lgkmcnt(5)
	v_mfma_f32_32x32x16_f16 v[18:33], v[122:125], v[50:53], v[2:17]
	ds_read_b128 v[244:247], v179 offset:17088
	v_cvt_pk_f16_f32 v156, v34, v35
	v_cvt_pk_f16_f32 v157, v36, v37
	s_waitcnt lgkmcnt(5)
	v_mfma_f32_32x32x16_f16 v[18:33], v[98:101], v[54:57], v[18:33]
	ds_read_b128 v[34:37], v179 offset:17120
	v_exp_f16_e64 v50, v156 clamp
	v_exp_f16_e64 v51, v157 clamp
	v_exp_f16_sdwa v50, v156 clamp dst_sel:WORD_1 dst_unused:UNUSED_PRESERVE src0_sel:WORD_1
	v_exp_f16_sdwa v51, v157 clamp dst_sel:WORD_1 dst_unused:UNUSED_PRESERVE src0_sel:WORD_1
	s_nop 0
	s_waitcnt lgkmcnt(5)
	v_mfma_f32_32x32x16_f16 v[18:33], v[114:117], v[58:61], v[18:33]
	ds_read_b128 v[248:251], v179 offset:17152
	v_pk_fma_f16 v51, v51, s55, v233 op_sel_hi:[1,0,0]
	v_pk_fma_f16 v50, v50, s55, v233 op_sel_hi:[1,0,0]
	v_pk_max_f16 v51, v157, v51
	v_pk_max_f16 v50, v156, v50
	s_waitcnt lgkmcnt(5)
	v_mfma_f32_32x32x16_f16 v[18:33], v[86:89], v[62:65], v[18:33]
	ds_read_b128 v[252:255], v179 offset:17184
	v_cvt_pk_f16_f32 v52, v38, v39
	v_cvt_pk_f16_f32 v53, v40, v41
	s_waitcnt lgkmcnt(5)
	v_mfma_f32_32x32x16_f16 v[18:33], v[126:129], v[170:173], v[18:33]
	ds_read_b128 v[38:41], v179 offset:17216
	v_exp_f16_e64 v54, v52 clamp
	v_exp_f16_e64 v55, v53 clamp
	v_exp_f16_sdwa v54, v52 clamp dst_sel:WORD_1 dst_unused:UNUSED_PRESERVE src0_sel:WORD_1
	v_exp_f16_sdwa v55, v53 clamp dst_sel:WORD_1 dst_unused:UNUSED_PRESERVE src0_sel:WORD_1
	s_nop 0
	s_waitcnt lgkmcnt(5)
	v_mfma_f32_32x32x16_f16 v[18:33], v[90:93], v[240:243], v[18:33]
	ds_read_b128 v[170:173], v179 offset:17248
	v_pk_fma_f16 v55, v55, s55, v233 op_sel_hi:[1,0,0]
	v_pk_fma_f16 v54, v54, s55, v233 op_sel_hi:[1,0,0]
	v_pk_max_f16 v53, v53, v55
	v_pk_max_f16 v52, v52, v54
	s_waitcnt lgkmcnt(5)
	v_mfma_f32_32x32x16_f16 v[18:33], v[118:121], v[244:247], v[18:33]
	ds_read_b128 v[240:243], v179 offset:17280
	v_cvt_pk_f16_f32 v156, v42, v43
	v_cvt_pk_f16_f32 v157, v44, v45
	v_mfma_f32_16x16x32_f16 v[62:65], v[70:73], v[50:53], 0
	s_waitcnt lgkmcnt(5)
	v_mfma_f32_32x32x16_f16 v[18:33], v[78:81], v[34:37], v[18:33]
	ds_read_b128 v[42:45], v179 offset:17312
	v_exp_f16_e64 v244, v156 clamp
	v_exp_f16_e64 v245, v157 clamp
	v_exp_f16_sdwa v244, v156 clamp dst_sel:WORD_1 dst_unused:UNUSED_PRESERVE src0_sel:WORD_1
	v_exp_f16_sdwa v245, v157 clamp dst_sel:WORD_1 dst_unused:UNUSED_PRESERVE src0_sel:WORD_1
	s_nop 0
	s_waitcnt lgkmcnt(5)
	v_mfma_f32_32x32x16_f16 v[18:33], v[102:105], v[248:251], v[18:33]
	ds_read_b128 v[34:37], v179 offset:17344
	v_pk_fma_f16 v245, v245, s55, v233 op_sel_hi:[1,0,0]
	s_nop 0
	v_pk_max_f16 v245, v157, v245
	v_pk_fma_f16 v157, v244, s55, v233 op_sel_hi:[1,0,0]
	s_nop 0
	v_pk_max_f16 v244, v156, v157
	s_waitcnt lgkmcnt(5)
	v_mfma_f32_32x32x16_f16 v[18:33], v[74:77], v[252:255], v[18:33]
	ds_read_b128 v[248:251], v179 offset:17376
	v_cvt_pk_f16_f32 v46, v46, v47
	v_cvt_pk_f16_f32 v47, v48, v49
	s_waitcnt lgkmcnt(5)
	v_mfma_f32_32x32x16_f16 v[18:33], v[106:109], v[38:41], v[18:33]
	v_exp_f16_e64 v48, v46 clamp
	v_exp_f16_e64 v49, v47 clamp
	v_exp_f16_sdwa v48, v46 clamp dst_sel:WORD_1 dst_unused:UNUSED_PRESERVE src0_sel:WORD_1
	v_exp_f16_sdwa v49, v47 clamp dst_sel:WORD_1 dst_unused:UNUSED_PRESERVE src0_sel:WORD_1
	s_nop 0
	s_waitcnt lgkmcnt(4)
	v_mfma_f32_32x32x16_f16 v[18:33], v[82:85], v[170:173], v[18:33]
	v_pk_fma_f16 v38, v49, s55, v233 op_sel_hi:[1,0,0]
	s_nop 0
	v_pk_max_f16 v247, v47, v38
	v_pk_fma_f16 v38, v48, s55, v233 op_sel_hi:[1,0,0]
	s_nop 0
	v_pk_max_f16 v246, v46, v38
	s_waitcnt lgkmcnt(3)
	v_mfma_f32_32x32x16_f16 v[18:33], v[110:113], v[240:243], v[18:33]
	s_waitcnt vmcnt(2)
	v_pk_add_f16 v40, v166, v146
	v_pk_add_f16 v41, v167, v147
	s_nop 0
	v_pk_mul_f16 v38, v168, v148 clamp
	v_pk_mul_f16 v39, v169, v149 clamp
	v_pk_max_f16 v38, v40, v38
	v_pk_max_f16 v39, v41, v39
	ds_write_b64 v189, v[38:39] offset:50688
	v_mfma_f32_16x16x32_f16 v[62:65], v[66:69], v[244:247], v[62:65]
	s_waitcnt lgkmcnt(3)
	v_mfma_f32_32x32x16_f16 v[18:33], v[94:97], v[42:45], v[18:33]
	v_pk_add_f16 v40, v166, v138
	v_pk_add_f16 v41, v167, v139
	s_nop 0
	v_pk_mul_f16 v38, v168, v140 clamp
	v_pk_mul_f16 v39, v169, v141 clamp
	v_pk_max_f16 v38, v40, v38
	v_pk_max_f16 v39, v41, v39
	ds_write_b64 v189, v[38:39] offset:51216
	s_waitcnt lgkmcnt(3)
	v_mfma_f32_32x32x16_f16 v[18:33], v[134:137], v[34:37], v[18:33]
	v_pk_add_f16 v40, v166, v150
	v_pk_add_f16 v41, v167, v151
	s_nop 0
	v_pk_mul_f16 v38, v168, v152 clamp
	v_pk_mul_f16 v39, v169, v153 clamp
	v_pk_max_f16 v38, v40, v38
	v_pk_max_f16 v39, v41, v39
	ds_write_b64 v189, v[38:39] offset:51744
	s_waitcnt lgkmcnt(3)
	v_mfma_f32_32x32x16_f16 v[18:33], v[130:133], v[248:251], v[18:33]
	v_pk_add_f16 v36, v166, v142
	v_pk_add_f16 v37, v167, v143
	s_nop 0
	v_pk_mul_f16 v34, v168, v144 clamp
	v_pk_mul_f16 v35, v169, v145 clamp
	v_pk_max_f16 v34, v36, v34
	v_pk_max_f16 v35, v37, v35
	ds_write_b64 v189, v[34:35] offset:52272
	ds_write2_b32 v206, v62, v63 offset1:1
	s_and_saveexec_b64 s[30:31], s[0:1]
	ds_write2_b32 v206, v64, v65 offset0:2 offset1:3
	s_or_b64 exec, exec, s[30:31]
	s_add_i32 s34, s34, 1
	s_sub_i32 s30, 0x7d, s34
	s_mul_i32 s30, s30, 6
	s_ashr_i32 s31, s30, 31
	s_add_u32 s28, s28, s30
	s_addc_u32 s29, s29, s31
	s_and_b64 vcc, exec, s[8:9]
	s_waitcnt lgkmcnt(0)
	s_barrier
	ds_read_b128 v[50:53], v179 offset:33792
	ds_read_b128 v[54:57], v179 offset:33824
	ds_read_b128 v[58:61], v179 offset:33856
	s_cbranch_vccnz .LBB1_136
	s_cmp_eq_u32 s41, 0
	s_cbranch_scc1 .LBB1_132
	s_and_saveexec_b64 s[30:31], s[6:7]
	s_cbranch_execz .LBB1_131
	ds_read2_b32 v[34:35], v180 offset1:224
	v_add_u32_e32 v36, 0x700, v180
	ds_read2_b32 v[36:37], v36 offset1:224
	v_add_u32_e32 v38, 0xe00, v180
	s_lshl_b32 s35, s56, 28
	s_waitcnt lgkmcnt(1)
	v_add_f32_e32 v34, 0, v34
	v_add_f32_e32 v40, v34, v35
	ds_read2_b32 v[34:35], v38 offset1:224
	v_add_u32_e32 v38, 0x1500, v180
	ds_read2_b32 v[38:39], v38 offset1:224
	s_waitcnt lgkmcnt(2)
	v_add_f32_e32 v36, v40, v36
	v_add_f32_e32 v36, v36, v37
	s_waitcnt lgkmcnt(1)
	v_add_f32_e32 v34, v36, v34
	s_add_i32 s35, s35, 0xf0000000
	v_add_f32_e32 v34, v34, v35
	s_ashr_i32 s35, s35, 31
	s_waitcnt lgkmcnt(0)
	v_add_f32_e32 v34, v34, v38
	s_and_b32 s35, s35, 0x1800
	v_add_f32_e32 v34, v34, v39
	v_add_u32_e32 v35, s35, v232
	ds_write_b32 v35, v34 offset:896

.LBB1_145:
	v_lshl_add_u64 v[166:167], s[20:21], 4, v[154:155]
	global_load_dwordx4 v[154:157], v[166:167], off
	ds_read_b128 v[62:65], v179 offset:33888
	ds_read_b128 v[168:171], v179 offset:33920
	ds_read_b128 v[240:243], v179 offset:33952
	s_waitcnt lgkmcnt(5)
	v_mfma_f32_32x32x16_f16 v[34:49], v[122:125], v[50:53], v[2:17]
	ds_read_b128 v[244:247], v179 offset:33984
	v_cvt_pk_f16_f32 v172, v18, v19
	v_cvt_pk_f16_f32 v173, v20, v21
	s_waitcnt lgkmcnt(5)
	v_mfma_f32_32x32x16_f16 v[34:49], v[98:101], v[54:57], v[34:49]
	ds_read_b128 v[18:21], v179 offset:34016
	v_exp_f16_e64 v50, v172 clamp
	v_exp_f16_e64 v51, v173 clamp
	v_exp_f16_sdwa v50, v172 clamp dst_sel:WORD_1 dst_unused:UNUSED_PRESERVE src0_sel:WORD_1
	v_exp_f16_sdwa v51, v173 clamp dst_sel:WORD_1 dst_unused:UNUSED_PRESERVE src0_sel:WORD_1
	s_nop 0
	s_waitcnt lgkmcnt(5)
	v_mfma_f32_32x32x16_f16 v[34:49], v[114:117], v[58:61], v[34:49]
	ds_read_b128 v[248:251], v179 offset:34048
	v_pk_fma_f16 v51, v51, s55, v233 op_sel_hi:[1,0,0]
	v_pk_fma_f16 v50, v50, s55, v233 op_sel_hi:[1,0,0]
	v_pk_max_f16 v51, v173, v51
	v_pk_max_f16 v50, v172, v50
	s_waitcnt lgkmcnt(5)
	v_mfma_f32_32x32x16_f16 v[34:49], v[86:89], v[62:65], v[34:49]
	ds_read_b128 v[252:255], v179 offset:34080
	v_cvt_pk_f16_f32 v52, v22, v23
	v_cvt_pk_f16_f32 v53, v24, v25
	s_waitcnt lgkmcnt(5)
	v_mfma_f32_32x32x16_f16 v[34:49], v[126:129], v[168:171], v[34:49]
	ds_read_b128 v[22:25], v179 offset:34112
	v_exp_f16_e64 v54, v52 clamp
	v_exp_f16_e64 v55, v53 clamp
	v_exp_f16_sdwa v54, v52 clamp dst_sel:WORD_1 dst_unused:UNUSED_PRESERVE src0_sel:WORD_1
	v_exp_f16_sdwa v55, v53 clamp dst_sel:WORD_1 dst_unused:UNUSED_PRESERVE src0_sel:WORD_1
	s_nop 0
	s_waitcnt lgkmcnt(5)
	v_mfma_f32_32x32x16_f16 v[34:49], v[90:93], v[240:243], v[34:49]
	ds_read_b128 v[168:171], v179 offset:34144
	v_pk_fma_f16 v55, v55, s55, v233 op_sel_hi:[1,0,0]
	v_pk_fma_f16 v54, v54, s55, v233 op_sel_hi:[1,0,0]
	v_pk_max_f16 v53, v53, v55
	v_pk_max_f16 v52, v52, v54
	s_waitcnt lgkmcnt(5)
	v_mfma_f32_32x32x16_f16 v[34:49], v[118:121], v[244:247], v[34:49]
	ds_read_b128 v[240:243], v179 offset:34176
	v_cvt_pk_f16_f32 v172, v26, v27
	v_cvt_pk_f16_f32 v173, v28, v29
	v_mfma_f32_16x16x32_f16 v[62:65], v[70:73], v[50:53], 0
	s_waitcnt lgkmcnt(5)
	v_mfma_f32_32x32x16_f16 v[34:49], v[78:81], v[18:21], v[34:49]
	ds_read_b128 v[26:29], v179 offset:34208
	v_exp_f16_e64 v244, v172 clamp
	v_exp_f16_e64 v245, v173 clamp
	v_exp_f16_sdwa v244, v172 clamp dst_sel:WORD_1 dst_unused:UNUSED_PRESERVE src0_sel:WORD_1
	v_exp_f16_sdwa v245, v173 clamp dst_sel:WORD_1 dst_unused:UNUSED_PRESERVE src0_sel:WORD_1
	s_nop 0
	s_waitcnt lgkmcnt(5)
	v_mfma_f32_32x32x16_f16 v[34:49], v[102:105], v[248:251], v[34:49]
	ds_read_b128 v[18:21], v179 offset:34240
	v_pk_fma_f16 v245, v245, s55, v233 op_sel_hi:[1,0,0]
	s_nop 0
	v_pk_max_f16 v245, v173, v245
	v_pk_fma_f16 v173, v244, s55, v233 op_sel_hi:[1,0,0]
	s_nop 0
	v_pk_max_f16 v244, v172, v173
	s_waitcnt lgkmcnt(5)
	v_mfma_f32_32x32x16_f16 v[34:49], v[74:77], v[252:255], v[34:49]
	ds_read_b128 v[248:251], v179 offset:34272
	v_cvt_pk_f16_f32 v30, v30, v31
	v_cvt_pk_f16_f32 v31, v32, v33
	s_waitcnt lgkmcnt(5)
	v_mfma_f32_32x32x16_f16 v[34:49], v[106:109], v[22:25], v[34:49]
	v_exp_f16_e64 v32, v30 clamp
	v_exp_f16_e64 v33, v31 clamp
	v_exp_f16_sdwa v32, v30 clamp dst_sel:WORD_1 dst_unused:UNUSED_PRESERVE src0_sel:WORD_1
	v_exp_f16_sdwa v33, v31 clamp dst_sel:WORD_1 dst_unused:UNUSED_PRESERVE src0_sel:WORD_1
	s_nop 0
	s_waitcnt lgkmcnt(4)
	v_mfma_f32_32x32x16_f16 v[34:49], v[82:85], v[168:171], v[34:49]
	v_pk_fma_f16 v22, v33, s55, v233 op_sel_hi:[1,0,0]
	s_nop 0
	v_pk_max_f16 v247, v31, v22
	v_pk_fma_f16 v22, v32, s55, v233 op_sel_hi:[1,0,0]
	s_nop 0
	v_pk_max_f16 v246, v30, v22
	s_waitcnt lgkmcnt(3)
	v_mfma_f32_32x32x16_f16 v[34:49], v[110:113], v[240:243], v[34:49]
	s_waitcnt vmcnt(2)
	v_pk_add_f16 v24, v146, v158
	v_pk_add_f16 v25, v147, v159
	s_nop 0
	v_pk_mul_f16 v22, v160, v148 clamp
	v_pk_mul_f16 v23, v161, v149 clamp
	v_pk_max_f16 v22, v24, v22
	v_pk_max_f16 v23, v25, v23
	ds_write_b64 v189, v[22:23]
	v_mfma_f32_16x16x32_f16 v[62:65], v[66:69], v[244:247], v[62:65]
	s_waitcnt lgkmcnt(3)
	v_mfma_f32_32x32x16_f16 v[34:49], v[94:97], v[26:29], v[34:49]
	v_pk_add_f16 v24, v138, v158
	v_pk_add_f16 v25, v139, v159
	s_nop 0
	v_pk_mul_f16 v22, v160, v140 clamp
	v_pk_mul_f16 v23, v161, v141 clamp
	v_pk_max_f16 v22, v24, v22
	v_pk_max_f16 v23, v25, v23
	ds_write_b64 v189, v[22:23] offset:528
	s_waitcnt lgkmcnt(3)
	v_mfma_f32_32x32x16_f16 v[34:49], v[134:137], v[18:21], v[34:49]
	v_pk_add_f16 v24, v150, v158
	v_pk_add_f16 v25, v151, v159
	s_nop 0
	v_pk_mul_f16 v22, v160, v152 clamp
	v_pk_mul_f16 v23, v161, v153 clamp
	v_pk_max_f16 v22, v24, v22
	v_pk_max_f16 v23, v25, v23
	ds_write_b64 v189, v[22:23] offset:1056
	s_waitcnt lgkmcnt(3)
	v_mfma_f32_32x32x16_f16 v[34:49], v[130:133], v[248:251], v[34:49]
	v_pk_add_f16 v20, v142, v158
	v_pk_add_f16 v21, v143, v159
	s_nop 0
	v_pk_mul_f16 v18, v160, v144 clamp
	v_pk_mul_f16 v19, v161, v145 clamp
	v_pk_max_f16 v18, v20, v18
	v_pk_max_f16 v19, v21, v19
	ds_write_b64 v189, v[18:19] offset:1584
	ds_write2_b32 v201, v62, v63 offset1:1
	s_and_saveexec_b64 s[30:31], s[0:1]
	ds_write2_b32 v201, v64, v65 offset0:2 offset1:3
	s_or_b64 exec, exec, s[30:31]
	v_lshl_add_u64 v[166:167], s[20:21], 4, v[166:167]
	global_load_dwordx4 v[158:161], v[166:167], off
	ds_read_b128 v[50:53], v179 offset:50688
	ds_read_b128 v[54:57], v179 offset:50720
	ds_read_b128 v[58:61], v179 offset:50752
	ds_read_b128 v[62:65], v179 offset:50784
	ds_read_b128 v[168:171], v179 offset:50816
	ds_read_b128 v[240:243], v179 offset:50848
	s_waitcnt lgkmcnt(5)
	v_mfma_f32_32x32x16_f16 v[18:33], v[122:125], v[50:53], v[2:17]
	ds_read_b128 v[244:247], v179 offset:50880
	v_cvt_pk_f16_f32 v172, v34, v35
	v_cvt_pk_f16_f32 v173, v36, v37
	s_waitcnt lgkmcnt(5)
	v_mfma_f32_32x32x16_f16 v[18:33], v[98:101], v[54:57], v[18:33]
	ds_read_b128 v[34:37], v179 offset:50912
	v_exp_f16_e64 v50, v172 clamp
	v_exp_f16_e64 v51, v173 clamp
	v_exp_f16_sdwa v50, v172 clamp dst_sel:WORD_1 dst_unused:UNUSED_PRESERVE src0_sel:WORD_1
	v_exp_f16_sdwa v51, v173 clamp dst_sel:WORD_1 dst_unused:UNUSED_PRESERVE src0_sel:WORD_1
	s_nop 0
	s_waitcnt lgkmcnt(5)
	v_mfma_f32_32x32x16_f16 v[18:33], v[114:117], v[58:61], v[18:33]
	ds_read_b128 v[248:251], v179 offset:50944
	v_pk_fma_f16 v51, v51, s55, v233 op_sel_hi:[1,0,0]
	v_pk_fma_f16 v50, v50, s55, v233 op_sel_hi:[1,0,0]
	v_pk_max_f16 v51, v173, v51
	v_pk_max_f16 v50, v172, v50
	s_waitcnt lgkmcnt(5)
	v_mfma_f32_32x32x16_f16 v[18:33], v[86:89], v[62:65], v[18:33]
	ds_read_b128 v[252:255], v179 offset:50976
	v_cvt_pk_f16_f32 v52, v38, v39
	v_cvt_pk_f16_f32 v53, v40, v41
	s_waitcnt lgkmcnt(5)
	v_mfma_f32_32x32x16_f16 v[18:33], v[126:129], v[168:171], v[18:33]
	ds_read_b128 v[38:41], v179 offset:51008
	v_exp_f16_e64 v54, v52 clamp
	v_exp_f16_e64 v55, v53 clamp
	v_exp_f16_sdwa v54, v52 clamp dst_sel:WORD_1 dst_unused:UNUSED_PRESERVE src0_sel:WORD_1
	v_exp_f16_sdwa v55, v53 clamp dst_sel:WORD_1 dst_unused:UNUSED_PRESERVE src0_sel:WORD_1
	s_nop 0
	s_waitcnt lgkmcnt(5)
	v_mfma_f32_32x32x16_f16 v[18:33], v[90:93], v[240:243], v[18:33]
	ds_read_b128 v[168:171], v179 offset:51040
	v_pk_fma_f16 v55, v55, s55, v233 op_sel_hi:[1,0,0]
	v_pk_fma_f16 v54, v54, s55, v233 op_sel_hi:[1,0,0]
	v_pk_max_f16 v53, v53, v55
	v_pk_max_f16 v52, v52, v54
	s_waitcnt lgkmcnt(5)
	v_mfma_f32_32x32x16_f16 v[18:33], v[118:121], v[244:247], v[18:33]
	ds_read_b128 v[240:243], v179 offset:51072
	v_cvt_pk_f16_f32 v172, v42, v43
	v_cvt_pk_f16_f32 v173, v44, v45
	v_mfma_f32_16x16x32_f16 v[62:65], v[70:73], v[50:53], 0
	s_waitcnt lgkmcnt(5)
	v_mfma_f32_32x32x16_f16 v[18:33], v[78:81], v[34:37], v[18:33]
	ds_read_b128 v[42:45], v179 offset:51104
	v_exp_f16_e64 v244, v172 clamp
	v_exp_f16_e64 v245, v173 clamp
	v_exp_f16_sdwa v244, v172 clamp dst_sel:WORD_1 dst_unused:UNUSED_PRESERVE src0_sel:WORD_1
	v_exp_f16_sdwa v245, v173 clamp dst_sel:WORD_1 dst_unused:UNUSED_PRESERVE src0_sel:WORD_1
	s_nop 0
	s_waitcnt lgkmcnt(5)
	v_mfma_f32_32x32x16_f16 v[18:33], v[102:105], v[248:251], v[18:33]
	ds_read_b128 v[34:37], v179 offset:51136
	v_pk_fma_f16 v245, v245, s55, v233 op_sel_hi:[1,0,0]
	s_nop 0
	v_pk_max_f16 v245, v173, v245
	v_pk_fma_f16 v173, v244, s55, v233 op_sel_hi:[1,0,0]
	s_nop 0
	v_pk_max_f16 v244, v172, v173
	s_waitcnt lgkmcnt(5)
	v_mfma_f32_32x32x16_f16 v[18:33], v[74:77], v[252:255], v[18:33]
	ds_read_b128 v[248:251], v179 offset:51168
	v_cvt_pk_f16_f32 v46, v46, v47
	v_cvt_pk_f16_f32 v47, v48, v49
	s_waitcnt lgkmcnt(5)
	v_mfma_f32_32x32x16_f16 v[18:33], v[106:109], v[38:41], v[18:33]
	v_exp_f16_e64 v48, v46 clamp
	v_exp_f16_e64 v49, v47 clamp
	v_exp_f16_sdwa v48, v46 clamp dst_sel:WORD_1 dst_unused:UNUSED_PRESERVE src0_sel:WORD_1
	v_exp_f16_sdwa v49, v47 clamp dst_sel:WORD_1 dst_unused:UNUSED_PRESERVE src0_sel:WORD_1
	s_nop 0
	s_waitcnt lgkmcnt(4)
	v_mfma_f32_32x32x16_f16 v[18:33], v[82:85], v[168:171], v[18:33]
	v_pk_fma_f16 v38, v49, s55, v233 op_sel_hi:[1,0,0]
	s_nop 0
	v_pk_max_f16 v247, v47, v38
	v_pk_fma_f16 v38, v48, s55, v233 op_sel_hi:[1,0,0]
	s_nop 0
	v_pk_max_f16 v246, v46, v38
	s_waitcnt lgkmcnt(3)
	v_mfma_f32_32x32x16_f16 v[18:33], v[110:113], v[240:243], v[18:33]
	s_waitcnt vmcnt(2)
	v_pk_add_f16 v40, v146, v162
	v_pk_add_f16 v41, v147, v163
	s_nop 0
	v_pk_mul_f16 v38, v164, v148 clamp
	v_pk_mul_f16 v39, v165, v149 clamp
	v_pk_max_f16 v38, v40, v38
	v_pk_max_f16 v39, v41, v39
	ds_write_b64 v189, v[38:39] offset:16896
	v_mfma_f32_16x16x32_f16 v[62:65], v[66:69], v[244:247], v[62:65]
	s_waitcnt lgkmcnt(3)
	v_mfma_f32_32x32x16_f16 v[18:33], v[94:97], v[42:45], v[18:33]
	v_pk_add_f16 v40, v138, v162
	v_pk_add_f16 v41, v139, v163
	s_nop 0
	v_pk_mul_f16 v38, v164, v140 clamp
	v_pk_mul_f16 v39, v165, v141 clamp
	v_pk_max_f16 v38, v40, v38
	v_pk_max_f16 v39, v41, v39
	ds_write_b64 v189, v[38:39] offset:17424
	s_waitcnt lgkmcnt(3)
	v_mfma_f32_32x32x16_f16 v[18:33], v[134:137], v[34:37], v[18:33]
	v_pk_add_f16 v40, v150, v162
	v_pk_add_f16 v41, v151, v163
	s_nop 0
	v_pk_mul_f16 v38, v164, v152 clamp
	v_pk_mul_f16 v39, v165, v153 clamp
	v_pk_max_f16 v38, v40, v38
	v_pk_max_f16 v39, v41, v39
	ds_write_b64 v189, v[38:39] offset:17952
	s_waitcnt lgkmcnt(3)
	v_mfma_f32_32x32x16_f16 v[18:33], v[130:133], v[248:251], v[18:33]
	v_pk_add_f16 v36, v142, v162
	v_pk_add_f16 v37, v143, v163
	s_nop 0
	v_pk_mul_f16 v34, v164, v144 clamp
	v_pk_mul_f16 v35, v165, v145 clamp
	v_pk_max_f16 v34, v36, v34
	v_pk_max_f16 v35, v37, v35
	ds_write_b64 v189, v[34:35] offset:18480
	ds_write2_b32 v211, v62, v63 offset1:1
	s_and_saveexec_b64 s[30:31], s[0:1]
	ds_write2_b32 v211, v64, v65 offset0:2 offset1:3
	s_or_b64 exec, exec, s[30:31]
	s_add_i32 s35, s34, 1
	s_add_i32 s34, s56, 8
	s_cmp_eq_u32 s56, 8
	s_cselect_b64 vcc, -1, 0
	s_and_b64 s[30:31], vcc, exec
	v_lshl_add_u64 v[34:35], s[20:21], 4, v[166:167]
	s_cselect_b32 s20, s44, s20
	s_add_i32 s35, s35, 1
	s_and_b64 s[26:27], exec, s[26:27]
	s_cselect_b32 s30, s51, s35
	s_sub_i32 s26, 0x7e, s30
	s_mul_i32 s26, s26, 6
	s_ashr_i32 s27, s26, 31
	s_add_u32 s26, s28, s26
	s_addc_u32 s27, s29, s27
	s_add_i32 s31, s30, 1
	s_add_i32 s48, s48, 2
	s_add_i32 s54, s54, 16
	v_cndmask_b32_e32 v169, v35, v175, vcc
	v_cndmask_b32_e32 v168, v34, v174, vcc
	s_cmp_eq_u32 s34, 32
	s_waitcnt lgkmcnt(0)
	s_barrier
	s_cbranch_scc1 .LBB1_155
	ds_read_b128 v[50:53], v179
	ds_read_b128 v[54:57], v179 offset:32
	ds_read_b128 v[58:61], v179 offset:64
	s_mov_b32 s56, s34
	s_and_b64 vcc, exec, s[8:9]
	s_cbranch_vccz .LBB1_42
	s_branch .LBB1_50
.LBB1_155:
	ds_read_b128 v[50:53], v179
	ds_read_b128 v[54:57], v179 offset:32
	ds_read_b128 v[58:61], v179 offset:64
	s_and_b64 vcc, exec, s[24:25]
	s_cbranch_vccz .LBB1_164
	s_cmp_lg_u32 s41, 0
	s_cbranch_scc0 .LBB1_160
	s_and_saveexec_b64 s[12:13], s[6:7]
	s_cbranch_execz .LBB1_159
	ds_read2_b32 v[34:35], v200 offset1:224
	v_add_u32_e32 v36, 0x700, v200
	v_add_u32_e32 v38, 0xe00, v200
	ds_read2_b32 v[36:37], v36 offset1:224
	ds_read2_b32 v[38:39], v38 offset1:224
	s_waitcnt lgkmcnt(2)
	v_add_f32_e32 v34, 0, v34
	v_add_f32_e32 v40, v34, v35
	v_add_u32_e32 v34, 0x1500, v200
	ds_read2_b32 v[34:35], v34 offset1:224
	s_waitcnt lgkmcnt(2)
	v_add_f32_e32 v36, v40, v36
	v_add_f32_e32 v36, v36, v37
	s_waitcnt lgkmcnt(1)
	v_add_f32_e32 v36, v36, v38
	v_add_f32_e32 v36, v36, v39
	s_waitcnt lgkmcnt(0)
	v_add_f32_e32 v34, v36, v34
	v_add_f32_e32 v34, v34, v35
	v_mov_b32_e32 v35, 0x19080
	v_lshl_add_u32 v35, v177, 2, v35
	ds_write_b32 v35, v34

.LBB1_173:
	ds_read_b128 v[62:65], v179 offset:96
	ds_read_b128 v[162:165], v179 offset:128
	ds_read_b128 v[166:169], v179 offset:160
	s_waitcnt lgkmcnt(5)
	v_mfma_f32_32x32x16_f16 v[34:49], v[122:125], v[50:53], v[2:17]
	ds_read_b128 v[170:173], v179 offset:192
	v_cvt_pk_f16_f32 v174, v18, v19
	v_cvt_pk_f16_f32 v175, v20, v21
	s_waitcnt lgkmcnt(5)
	v_mfma_f32_32x32x16_f16 v[34:49], v[98:101], v[54:57], v[34:49]
	ds_read_b128 v[18:21], v179 offset:224
	v_exp_f16_e64 v50, v174 clamp
	v_exp_f16_e64 v51, v175 clamp
	v_exp_f16_sdwa v50, v174 clamp dst_sel:WORD_1 dst_unused:UNUSED_PRESERVE src0_sel:WORD_1
	v_exp_f16_sdwa v51, v175 clamp dst_sel:WORD_1 dst_unused:UNUSED_PRESERVE src0_sel:WORD_1
	s_nop 0
	s_waitcnt lgkmcnt(5)
	v_mfma_f32_32x32x16_f16 v[34:49], v[114:117], v[58:61], v[34:49]
	ds_read_b128 v[230:233], v179 offset:256
	s_movk_i32 s20, 0x3dc5
	v_mov_b32_e32 v199, 0xbdc5
	v_pk_fma_f16 v51, v51, s20, v199 op_sel_hi:[1,0,0]
	v_pk_fma_f16 v50, v50, s20, v199 op_sel_hi:[1,0,0]
	v_pk_max_f16 v51, v175, v51
	v_pk_max_f16 v50, v174, v50
	s_waitcnt lgkmcnt(5)
	v_mfma_f32_32x32x16_f16 v[34:49], v[86:89], v[62:65], v[34:49]
	ds_read_b128 v[234:237], v179 offset:288
	v_cvt_pk_f16_f32 v52, v22, v23
	v_cvt_pk_f16_f32 v53, v24, v25
	s_waitcnt lgkmcnt(5)
	v_mfma_f32_32x32x16_f16 v[34:49], v[126:129], v[162:165], v[34:49]
	ds_read_b128 v[22:25], v179 offset:320
	v_exp_f16_e64 v54, v52 clamp
	v_exp_f16_e64 v55, v53 clamp
	v_exp_f16_sdwa v54, v52 clamp dst_sel:WORD_1 dst_unused:UNUSED_PRESERVE src0_sel:WORD_1
	v_exp_f16_sdwa v55, v53 clamp dst_sel:WORD_1 dst_unused:UNUSED_PRESERVE src0_sel:WORD_1
	s_nop 0
	s_waitcnt lgkmcnt(5)
	v_mfma_f32_32x32x16_f16 v[34:49], v[90:93], v[166:169], v[34:49]
	ds_read_b128 v[162:165], v179 offset:352
	v_pk_fma_f16 v55, v55, s20, v199 op_sel_hi:[1,0,0]
	v_pk_fma_f16 v54, v54, s20, v199 op_sel_hi:[1,0,0]
	v_pk_max_f16 v53, v53, v55
	v_pk_max_f16 v52, v52, v54
	s_waitcnt lgkmcnt(5)
	v_mfma_f32_32x32x16_f16 v[34:49], v[118:121], v[170:173], v[34:49]
	ds_read_b128 v[166:169], v179 offset:384
	v_cvt_pk_f16_f32 v170, v26, v27
	v_cvt_pk_f16_f32 v171, v28, v29
	v_mfma_f32_16x16x32_f16 v[62:65], v[70:73], v[50:53], 0
	s_waitcnt lgkmcnt(5)
	v_mfma_f32_32x32x16_f16 v[34:49], v[78:81], v[18:21], v[34:49]
	ds_read_b128 v[26:29], v179 offset:416
	v_exp_f16_e64 v172, v170 clamp
	v_exp_f16_e64 v173, v171 clamp
	v_exp_f16_sdwa v172, v170 clamp dst_sel:WORD_1 dst_unused:UNUSED_PRESERVE src0_sel:WORD_1
	v_exp_f16_sdwa v173, v171 clamp dst_sel:WORD_1 dst_unused:UNUSED_PRESERVE src0_sel:WORD_1
	s_nop 0
	s_waitcnt lgkmcnt(5)
	v_mfma_f32_32x32x16_f16 v[34:49], v[102:105], v[230:233], v[34:49]
	ds_read_b128 v[18:21], v179 offset:448
	v_pk_fma_f16 v173, v173, s20, v199 op_sel_hi:[1,0,0]
	v_pk_fma_f16 v172, v172, s20, v199 op_sel_hi:[1,0,0]
	v_pk_max_f16 v171, v171, v173
	v_pk_max_f16 v170, v170, v172
	s_waitcnt lgkmcnt(5)
	v_mfma_f32_32x32x16_f16 v[34:49], v[74:77], v[234:237], v[34:49]
	ds_read_b128 v[230:233], v179 offset:480
	v_cvt_pk_f16_f32 v30, v30, v31
	v_cvt_pk_f16_f32 v31, v32, v33
	s_waitcnt lgkmcnt(5)
	v_mfma_f32_32x32x16_f16 v[34:49], v[106:109], v[22:25], v[34:49]
	v_exp_f16_e64 v32, v30 clamp
	v_exp_f16_e64 v33, v31 clamp
	v_exp_f16_sdwa v32, v30 clamp dst_sel:WORD_1 dst_unused:UNUSED_PRESERVE src0_sel:WORD_1
	v_exp_f16_sdwa v33, v31 clamp dst_sel:WORD_1 dst_unused:UNUSED_PRESERVE src0_sel:WORD_1
	s_nop 0
	s_waitcnt lgkmcnt(4)
	v_mfma_f32_32x32x16_f16 v[34:49], v[82:85], v[162:165], v[34:49]
	v_pk_fma_f16 v22, v33, s20, v199 op_sel_hi:[1,0,0]
	s_nop 0
	v_pk_max_f16 v173, v31, v22
	v_pk_fma_f16 v22, v32, s20, v199 op_sel_hi:[1,0,0]
	s_nop 0
	v_pk_max_f16 v172, v30, v22
	s_waitcnt lgkmcnt(3)
	v_mfma_f32_32x32x16_f16 v[34:49], v[110:113], v[166:169], v[34:49]
	s_waitcnt vmcnt(1)
	v_pk_add_f16 v24, v146, v154
	v_pk_add_f16 v25, v147, v155
	s_nop 0
	v_pk_mul_f16 v22, v156, v148 clamp
	v_pk_mul_f16 v23, v157, v149 clamp
	v_pk_max_f16 v22, v24, v22
	v_pk_max_f16 v23, v25, v23
	ds_write_b64 v189, v[22:23] offset:33792
	v_mfma_f32_16x16x32_f16 v[62:65], v[66:69], v[170:173], v[62:65]
	s_waitcnt lgkmcnt(3)
	v_mfma_f32_32x32x16_f16 v[34:49], v[94:97], v[26:29], v[34:49]
	v_pk_add_f16 v24, v138, v154
	v_pk_add_f16 v25, v139, v155
	s_nop 0
	v_pk_mul_f16 v22, v156, v140 clamp
	v_pk_mul_f16 v23, v157, v141 clamp
	v_pk_max_f16 v22, v24, v22
	v_pk_max_f16 v23, v25, v23
	ds_write_b64 v189, v[22:23] offset:34320
	s_waitcnt lgkmcnt(3)
	v_mfma_f32_32x32x16_f16 v[34:49], v[134:137], v[18:21], v[34:49]
	v_pk_add_f16 v24, v150, v154
	v_pk_add_f16 v25, v151, v155
	s_nop 0
	v_pk_mul_f16 v22, v156, v152 clamp
	v_pk_mul_f16 v23, v157, v153 clamp
	v_pk_max_f16 v22, v24, v22
	v_pk_max_f16 v23, v25, v23
	ds_write_b64 v189, v[22:23] offset:34848
	s_waitcnt lgkmcnt(3)
	v_mfma_f32_32x32x16_f16 v[34:49], v[130:133], v[230:233], v[34:49]
	v_pk_add_f16 v20, v142, v154
	v_pk_add_f16 v21, v143, v155
	s_nop 0
	v_pk_mul_f16 v18, v156, v144 clamp
	v_pk_mul_f16 v19, v157, v145 clamp
	v_pk_max_f16 v18, v20, v18
	v_pk_max_f16 v19, v21, v19
	ds_write_b64 v189, v[18:19] offset:35376
	ds_write2_b32 v229, v62, v63 offset1:1
	s_and_saveexec_b64 s[20:21], s[0:1]
	ds_write2_b32 v229, v64, v65 offset0:2 offset1:3
	s_or_b64 exec, exec, s[20:21]
	ds_read_b128 v[50:53], v179 offset:16896
	ds_read_b128 v[54:57], v179 offset:16928
	ds_read_b128 v[58:61], v179 offset:16960
	ds_read_b128 v[62:65], v179 offset:16992
	ds_read_b128 v[154:157], v179 offset:17024
	ds_read_b128 v[162:165], v179 offset:17056
	s_waitcnt lgkmcnt(5)
	v_mfma_f32_32x32x16_f16 v[18:33], v[122:125], v[50:53], v[2:17]
	ds_read_b128 v[166:169], v179 offset:17088
	v_cvt_pk_f16_f32 v174, v34, v35
	v_cvt_pk_f16_f32 v175, v36, v37
	s_waitcnt lgkmcnt(5)
	v_mfma_f32_32x32x16_f16 v[18:33], v[98:101], v[54:57], v[18:33]
	ds_read_b128 v[34:37], v179 offset:17120
	v_exp_f16_e64 v50, v174 clamp
	v_exp_f16_e64 v51, v175 clamp
	v_exp_f16_sdwa v50, v174 clamp dst_sel:WORD_1 dst_unused:UNUSED_PRESERVE src0_sel:WORD_1
	v_exp_f16_sdwa v51, v175 clamp dst_sel:WORD_1 dst_unused:UNUSED_PRESERVE src0_sel:WORD_1
	s_nop 0
	s_waitcnt lgkmcnt(5)
	v_mfma_f32_32x32x16_f16 v[18:33], v[114:117], v[58:61], v[18:33]
	ds_read_b128 v[170:173], v179 offset:17152
	s_movk_i32 s20, 0x3dc5
	v_mov_b32_e32 v199, 0xbdc5
	v_pk_fma_f16 v51, v51, s20, v199 op_sel_hi:[1,0,0]
	v_pk_fma_f16 v50, v50, s20, v199 op_sel_hi:[1,0,0]
	v_pk_max_f16 v51, v175, v51
	v_pk_max_f16 v50, v174, v50
	s_waitcnt lgkmcnt(5)
	v_mfma_f32_32x32x16_f16 v[18:33], v[86:89], v[62:65], v[18:33]
	ds_read_b128 v[228:231], v179 offset:17184
	v_cvt_pk_f16_f32 v52, v38, v39
	v_cvt_pk_f16_f32 v53, v40, v41
	s_waitcnt lgkmcnt(5)
	v_mfma_f32_32x32x16_f16 v[18:33], v[126:129], v[154:157], v[18:33]
	ds_read_b128 v[38:41], v179 offset:17216
	v_exp_f16_e64 v54, v52 clamp
	v_exp_f16_e64 v55, v53 clamp
	v_exp_f16_sdwa v54, v52 clamp dst_sel:WORD_1 dst_unused:UNUSED_PRESERVE src0_sel:WORD_1
	v_exp_f16_sdwa v55, v53 clamp dst_sel:WORD_1 dst_unused:UNUSED_PRESERVE src0_sel:WORD_1
	s_nop 0
	s_waitcnt lgkmcnt(5)
	v_mfma_f32_32x32x16_f16 v[18:33], v[90:93], v[162:165], v[18:33]
	ds_read_b128 v[154:157], v179 offset:17248
	v_pk_fma_f16 v55, v55, s20, v199 op_sel_hi:[1,0,0]
	v_pk_fma_f16 v54, v54, s20, v199 op_sel_hi:[1,0,0]
	v_pk_max_f16 v53, v53, v55
	v_pk_max_f16 v52, v52, v54
	s_waitcnt lgkmcnt(5)
	v_mfma_f32_32x32x16_f16 v[18:33], v[118:121], v[166:169], v[18:33]
	ds_read_b128 v[162:165], v179 offset:17280
	v_cvt_pk_f16_f32 v166, v42, v43
	v_cvt_pk_f16_f32 v167, v44, v45
	v_mfma_f32_16x16x32_f16 v[62:65], v[70:73], v[50:53], 0
	s_waitcnt lgkmcnt(5)
	v_mfma_f32_32x32x16_f16 v[18:33], v[78:81], v[34:37], v[18:33]
	ds_read_b128 v[42:45], v179 offset:17312
	v_exp_f16_e64 v168, v166 clamp
	v_exp_f16_e64 v169, v167 clamp
	v_exp_f16_sdwa v168, v166 clamp dst_sel:WORD_1 dst_unused:UNUSED_PRESERVE src0_sel:WORD_1
	v_exp_f16_sdwa v169, v167 clamp dst_sel:WORD_1 dst_unused:UNUSED_PRESERVE src0_sel:WORD_1
	s_nop 0
	s_waitcnt lgkmcnt(5)
	v_mfma_f32_32x32x16_f16 v[18:33], v[102:105], v[170:173], v[18:33]
	ds_read_b128 v[34:37], v179 offset:17344
	v_pk_fma_f16 v169, v169, s20, v199 op_sel_hi:[1,0,0]
	v_pk_fma_f16 v168, v168, s20, v199 op_sel_hi:[1,0,0]
	v_pk_max_f16 v167, v167, v169
	v_pk_max_f16 v166, v166, v168
	s_waitcnt lgkmcnt(5)
	v_mfma_f32_32x32x16_f16 v[18:33], v[74:77], v[228:231], v[18:33]
	ds_read_b128 v[170:173], v179 offset:17376
	v_cvt_pk_f16_f32 v46, v46, v47
	v_cvt_pk_f16_f32 v47, v48, v49
	s_waitcnt lgkmcnt(5)
	v_mfma_f32_32x32x16_f16 v[18:33], v[106:109], v[38:41], v[18:33]
	v_exp_f16_e64 v48, v46 clamp
	v_exp_f16_e64 v49, v47 clamp
	v_exp_f16_sdwa v48, v46 clamp dst_sel:WORD_1 dst_unused:UNUSED_PRESERVE src0_sel:WORD_1
	v_exp_f16_sdwa v49, v47 clamp dst_sel:WORD_1 dst_unused:UNUSED_PRESERVE src0_sel:WORD_1
	s_nop 0
	s_waitcnt lgkmcnt(4)
	v_mfma_f32_32x32x16_f16 v[18:33], v[82:85], v[154:157], v[18:33]
	v_pk_fma_f16 v38, v49, s20, v199 op_sel_hi:[1,0,0]
	s_nop 0
	v_pk_max_f16 v169, v47, v38
	v_pk_fma_f16 v38, v48, s20, v199 op_sel_hi:[1,0,0]
	s_nop 0
	v_pk_max_f16 v168, v46, v38
	s_waitcnt lgkmcnt(3)
	v_mfma_f32_32x32x16_f16 v[18:33], v[110:113], v[162:165], v[18:33]
	s_waitcnt vmcnt(0)
	v_pk_add_f16 v40, v146, v158
	v_pk_add_f16 v41, v147, v159
	s_nop 0
	v_pk_mul_f16 v38, v160, v148 clamp
	v_pk_mul_f16 v39, v161, v149 clamp
	v_pk_max_f16 v38, v40, v38
	v_pk_max_f16 v39, v41, v39
	ds_write_b64 v189, v[38:39] offset:50688
	v_mfma_f32_16x16x32_f16 v[62:65], v[66:69], v[166:169], v[62:65]
	s_waitcnt lgkmcnt(3)
	v_mfma_f32_32x32x16_f16 v[18:33], v[94:97], v[42:45], v[18:33]
	v_pk_add_f16 v40, v138, v158
	v_pk_add_f16 v41, v139, v159
	s_nop 0
	v_pk_mul_f16 v38, v160, v140 clamp
	v_pk_mul_f16 v39, v161, v141 clamp
	v_pk_max_f16 v38, v40, v38
	v_pk_max_f16 v39, v41, v39
	ds_write_b64 v189, v[38:39] offset:51216
	s_waitcnt lgkmcnt(3)
	v_mfma_f32_32x32x16_f16 v[18:33], v[134:137], v[34:37], v[18:33]
	v_pk_add_f16 v40, v150, v158
	v_pk_add_f16 v41, v151, v159
	s_nop 0
	v_pk_mul_f16 v38, v160, v152 clamp
	v_pk_mul_f16 v39, v161, v153 clamp
	v_pk_max_f16 v38, v40, v38
	v_pk_max_f16 v39, v41, v39
	ds_write_b64 v189, v[38:39] offset:51744
	s_waitcnt lgkmcnt(3)
	v_mfma_f32_32x32x16_f16 v[18:33], v[130:133], v[170:173], v[18:33]
	v_pk_add_f16 v36, v142, v158
	v_pk_add_f16 v37, v143, v159
	s_nop 0
	v_pk_mul_f16 v34, v160, v144 clamp
	v_pk_mul_f16 v35, v161, v145 clamp
	v_pk_max_f16 v34, v36, v34
	v_pk_max_f16 v35, v37, v35
	ds_write_b64 v189, v[34:35] offset:52272
	ds_write2_b32 v206, v62, v63 offset1:1
	s_and_saveexec_b64 s[20:21], s[0:1]
	ds_write2_b32 v206, v64, v65 offset0:2 offset1:3
	s_or_b64 exec, exec, s[20:21]
	s_sub_i32 s20, 0x7c, s30
	s_mul_i32 s20, s20, 6
	s_ashr_i32 s21, s20, 31
	s_add_u32 s12, s12, s20
	s_addc_u32 s13, s13, s21
	s_and_b64 vcc, exec, s[8:9]
	s_waitcnt lgkmcnt(0)
	s_barrier
	s_cbranch_vccnz .LBB1_190
	s_cmp_lg_u32 s41, 0
	s_cbranch_scc0 .LBB1_186
	s_and_saveexec_b64 s[20:21], s[6:7]
	s_cbranch_execz .LBB1_185
	ds_read2_b32 v[34:35], v180 offset1:224
	v_add_u32_e32 v36, 0x700, v180
	v_add_u32_e32 v38, 0xe00, v180
	ds_read2_b32 v[36:37], v36 offset1:224
	ds_read2_b32 v[38:39], v38 offset1:224
	s_waitcnt lgkmcnt(2)
	v_add_f32_e32 v34, 0, v34
	v_add_f32_e32 v40, v34, v35
	v_add_u32_e32 v34, 0x1500, v180
	ds_read2_b32 v[34:35], v34 offset1:224
	s_waitcnt lgkmcnt(2)
	v_add_f32_e32 v36, v40, v36
	v_add_f32_e32 v36, v36, v37
	s_waitcnt lgkmcnt(1)
	v_add_f32_e32 v36, v36, v38
	v_add_f32_e32 v36, v36, v39
	s_waitcnt lgkmcnt(0)
	v_add_f32_e32 v34, v36, v34
	v_add_f32_e32 v34, v34, v35
	v_mov_b32_e32 v35, 0x19180
	v_lshl_add_u32 v35, v177, 2, v35
	ds_write_b32 v35, v34
